# attention loops: drop negm accumulator copies (use negm as SrcC), m0 save/restore, self-max canonicalisations, add-zero (exact trims)
# speedup vs baseline: 1.0198x; 1.0198x over previous
.LBB0_260:
	s_lshr_b32 s84, s21, 1
	s_bitcmp0_b32 s21, 0
	s_cselect_b32 s82, s49, s48
	s_lshl_b32 s0, s84, 7
	s_add_u32 s3, s52, s0
	s_addc_u32 s33, s53, 0
	s_add_u32 s39, s54, s0
	v_mov_b32_e32 v36, v0
	s_mov_b32 s38, s82
	s_mov_b32 s0, s4
	s_addc_u32 s43, s55, 0
	s_ashr_i32 s1, s0, 31
	v_readfirstlane_b32 s2, v36
	s_lshl_b64 s[34:35], s[0:1], 14
	s_lshl_b32 s1, s38, 8
	s_ashr_i32 s83, s2, 6
	s_ashr_i32 s36, s1, 31
	s_add_u32 s34, s34, s1
	s_addc_u32 s35, s35, s36
	s_lshl_b32 s46, s83, 5
	s_ashr_i32 s36, s46, 31
	s_add_u32 s34, s34, s46
	s_addc_u32 s35, s35, s36
	s_mul_i32 s36, s35, 0x1200
	s_mul_hi_u32 s37, s34, 0x1200
	s_add_i32 s37, s37, s36
	s_mul_i32 s36, s34, 0x1200
	s_add_u32 s36, s3, s36
	s_addc_u32 s37, s33, s37
	s_mul_hi_i32 s3, s0, 0x4800000
	s_mul_i32 s0, s0, 0x4800000
	v_and_b32_e32 v230, 63, v36
	s_add_u32 s42, s39, s0
	s_addc_u32 s43, s43, s3
	v_mul_u32_u24_e32 v2, 0x900, v230
	s_add_u32 s44, s62, s0
	v_lshlrev_b32_e32 v2, 1, v2
	s_addc_u32 s45, s63, s3
	v_lshl_add_u64 v[4:5], s[42:43], 0, v[2:3]
	s_lshl_b32 s42, s83, 3
	s_lshl_b32 s0, s83, 4
	v_bfe_u32 v2, v36, 2, 4
	s_ashr_i32 s43, s42, 31
	v_and_or_b32 v2, s0, 48, v2
	s_ashr_i32 s0, s2, 3
	v_lshl_add_u64 v[216:217], s[42:43], 1, v[4:5]
	s_and_b32 s42, s0, 0xffffffe0
	v_mul_u32_u24_e32 v2, 0x900, v2
	s_ashr_i32 s43, s42, 31
	s_lshl_b32 s0, s83, 10
	v_lshlrev_b32_e32 v2, 1, v2
	v_lshlrev_b32_e32 v232, 3, v36
	s_cmp_lg_u32 0, -1
	v_lshl_add_u64 v[4:5], s[44:45], 0, v[2:3]
	v_and_b32_e32 v233, 24, v232
	s_cselect_b32 s3, 0, 0
	v_and_b32_e32 v231, 31, v36
	v_lshl_add_u64 v[4:5], s[42:43], 1, v[4:5]
	v_lshlrev_b32_e32 v2, 1, v233
	s_add_i32 s76, s0, s3
	s_mov_b32 m0, s76
	s_nop 0
	global_load_lds_dwordx4 v[216:217], off
	v_lshl_add_u64 v[218:219], v[4:5], 0, v[2:3]
	s_add_i32 s77, s76, 0x6000
	s_mov_b32 m0, s77
	s_nop 0
	global_load_lds_dwordx4 v[218:219], off
	s_mov_b64 s[42:43], 0x80
	v_mul_u32_u24_e32 v2, 0x900, v231
	v_bfe_u32 v229, v36, 5, 1
	v_lshl_add_u64 v[220:221], v[218:219], 0, s[42:43]
	s_add_i32 s3, s76, 0x8000
	s_mov_b32 m0, s3
	s_nop 0
	global_load_lds_dwordx4 v[220:221], off
	v_lshlrev_b32_e32 v2, 1, v2
	v_lshl_add_u64 v[4:5], v[216:217], 0, s[26:27]
	s_add_i32 s3, s76, 0x2000
	s_mov_b32 m0, s3
	s_nop 0
	global_load_lds_dwordx4 v[4:5], off
	v_lshl_or_b32 v2, v229, 4, v2
	global_load_dwordx4 v[154:157], v2, s[36:37]
	global_load_dwordx4 v[150:153], v2, s[36:37] offset:32
	global_load_dwordx4 v[146:149], v2, s[36:37] offset:64
	global_load_dwordx4 v[142:145], v2, s[36:37] offset:96
	s_mov_b64 s[36:37], 0x48080
	v_lshlrev_b32_e32 v2, 10, v229
	v_lshlrev_b32_e32 v4, 4, v231
	v_add3_u32 v240, 0, v2, v4
	v_lshl_add_u64 v[4:5], v[216:217], 0, s[28:29]
	s_add_i32 s3, s76, 0x4000
	v_lshl_add_u64 v[8:9], v[218:219], 0, s[36:37]
	s_mov_b32 m0, s3
	s_nop 0
	global_load_lds_dwordx4 v[4:5], off
	s_add_i32 s33, s76, 0xa000
	v_lshl_add_u64 v[6:7], v[218:219], 0, s[26:27]
	s_mov_b32 m0, s33
	s_nop 0
	global_load_lds_dwordx4 v[6:7], off
	s_add_i32 s39, s76, 0xc000
	s_mov_b32 m0, s39
	s_nop 0
	global_load_lds_dwordx4 v[8:9], off
	s_waitcnt vmcnt(6) lgkmcnt(0)
	s_barrier
	ds_read_b128 v[4:7], v240
	ds_read_b128 v[8:11], v240 offset:512
	ds_read_b128 v[38:41], v240 offset:2048
	ds_read_b128 v[42:45], v240 offset:2560
	s_add_i32 s3, s1, 0x100
	s_ashr_i32 s85, s3, 6
	v_lshlrev_b32_e32 v239, 2, v229
	v_or_b32_e32 v238, s46, v231
	s_cmp_gt_i32 s85, 4
	s_waitcnt vmcnt(3) lgkmcnt(3)
	v_mfma_f32_32x32x16_bf16 v[20:35], v[4:7], v[154:157], 0
	s_waitcnt lgkmcnt(2)
	v_mfma_f32_32x32x16_bf16 v[4:19], v[8:11], v[154:157], 0
	s_waitcnt vmcnt(2) lgkmcnt(1)
	v_mfma_f32_32x32x16_bf16 v[20:35], v[38:41], v[150:153], v[20:35]
	s_waitcnt lgkmcnt(0)
	v_mfma_f32_32x32x16_bf16 v[4:19], v[42:45], v[150:153], v[4:19]
	ds_read_b128 v[38:41], v240 offset:4096
	ds_read_b128 v[42:45], v240 offset:4608
	s_waitcnt vmcnt(1) lgkmcnt(1)
	v_mfma_f32_32x32x16_bf16 v[20:35], v[38:41], v[146:149], v[20:35]
	s_waitcnt lgkmcnt(0)
	v_mfma_f32_32x32x16_bf16 v[4:19], v[42:45], v[146:149], v[4:19]
	ds_read_b128 v[38:41], v240 offset:6144
	ds_read_b128 v[42:45], v240 offset:6656
	s_waitcnt vmcnt(0) lgkmcnt(1)
	v_mfma_f32_32x32x16_bf16 v[20:35], v[38:41], v[142:145], v[20:35]
	s_waitcnt lgkmcnt(0)
	v_mfma_f32_32x32x16_bf16 v[4:19], v[42:45], v[142:145], v[4:19]
	s_nop 15
	s_nop 7
	s_cbranch_scc1 .LBB0_262
	v_subrev_u32_e32 v2, s1, v239
	v_or_b32_e32 v37, 32, v2
	v_cmp_le_i32_e32 vcc, v37, v238
	v_or_b32_e32 v37, 33, v2
	s_nop 6
	v_cndmask_b32_e32 v4, v227, v4, vcc
	v_cmp_lt_i32_e32 vcc, v2, v238
	s_nop 1
	v_cndmask_b32_e32 v21, v227, v21, vcc
	v_cmp_le_i32_e32 vcc, v2, v238
	s_nop 1
	v_cndmask_b32_e32 v20, v227, v20, vcc
	v_cmp_le_i32_e32 vcc, v37, v238
	v_or_b32_e32 v37, 2, v2
	s_nop 0
	v_cndmask_b32_e32 v5, v227, v5, vcc
	v_cmp_le_i32_e32 vcc, v37, v238
	v_or_b32_e32 v37, 34, v2
	s_nop 0
	v_cndmask_b32_e32 v22, v227, v22, vcc
	v_cmp_le_i32_e32 vcc, v37, v238
	v_or_b32_e32 v37, 3, v2
	s_nop 0
	v_cndmask_b32_e32 v6, v227, v6, vcc
	v_cmp_le_i32_e32 vcc, v37, v238
	v_or_b32_e32 v37, 35, v2
	s_nop 0
	v_cndmask_b32_e32 v23, v227, v23, vcc
	v_cmp_le_i32_e32 vcc, v37, v238
	v_or_b32_e32 v37, 8, v2
	s_nop 0
	v_cndmask_b32_e32 v7, v227, v7, vcc
	v_cmp_le_i32_e32 vcc, v37, v238
	v_or_b32_e32 v37, 40, v2
	s_nop 0
	v_cndmask_b32_e32 v24, v227, v24, vcc
	v_cmp_le_i32_e32 vcc, v37, v238
	v_or_b32_e32 v37, 9, v2
	s_nop 0
	v_cndmask_b32_e32 v8, v227, v8, vcc
	v_cmp_le_i32_e32 vcc, v37, v238
	v_or_b32_e32 v37, 41, v2
	s_nop 0
	v_cndmask_b32_e32 v25, v227, v25, vcc
	v_cmp_le_i32_e32 vcc, v37, v238
	v_or_b32_e32 v37, 10, v2
	s_nop 0
	v_cndmask_b32_e32 v9, v227, v9, vcc
	v_cmp_le_i32_e32 vcc, v37, v238
	v_or_b32_e32 v37, 42, v2
	s_nop 0
	v_cndmask_b32_e32 v26, v227, v26, vcc
	v_cmp_le_i32_e32 vcc, v37, v238
	v_or_b32_e32 v37, 11, v2
	s_nop 0
	v_cndmask_b32_e32 v10, v227, v10, vcc
	v_cmp_le_i32_e32 vcc, v37, v238
	v_or_b32_e32 v37, 43, v2
	s_nop 0
	v_cndmask_b32_e32 v27, v227, v27, vcc
	v_cmp_le_i32_e32 vcc, v37, v238
	v_or_b32_e32 v37, 16, v2
	s_nop 0
	v_cndmask_b32_e32 v11, v227, v11, vcc
	v_cmp_le_i32_e32 vcc, v37, v238
	v_or_b32_e32 v37, 48, v2
	s_nop 0
	v_cndmask_b32_e32 v28, v227, v28, vcc
	v_cmp_le_i32_e32 vcc, v37, v238
	v_or_b32_e32 v37, 17, v2
	s_nop 0
	v_cndmask_b32_e32 v12, v227, v12, vcc
	v_cmp_le_i32_e32 vcc, v37, v238
	v_or_b32_e32 v37, 49, v2
	s_nop 0
	v_cndmask_b32_e32 v29, v227, v29, vcc
	v_cmp_le_i32_e32 vcc, v37, v238
	v_or_b32_e32 v37, 18, v2
	s_nop 0
	v_cndmask_b32_e32 v13, v227, v13, vcc
	v_cmp_le_i32_e32 vcc, v37, v238
	v_or_b32_e32 v37, 50, v2
	s_nop 0
	v_cndmask_b32_e32 v30, v227, v30, vcc
	v_cmp_le_i32_e32 vcc, v37, v238
	v_or_b32_e32 v37, 19, v2
	s_nop 0
	v_cndmask_b32_e32 v14, v227, v14, vcc
	v_cmp_le_i32_e32 vcc, v37, v238
	v_or_b32_e32 v37, 51, v2
	s_nop 0
	v_cndmask_b32_e32 v31, v227, v31, vcc
	v_cmp_le_i32_e32 vcc, v37, v238
	v_or_b32_e32 v37, 24, v2
	s_nop 0
	v_cndmask_b32_e32 v15, v227, v15, vcc
	v_cmp_le_i32_e32 vcc, v37, v238
	v_or_b32_e32 v37, 56, v2
	s_nop 0
	v_cndmask_b32_e32 v32, v227, v32, vcc
	v_cmp_le_i32_e32 vcc, v37, v238
	v_or_b32_e32 v37, 25, v2
	s_nop 0
	v_cndmask_b32_e32 v16, v227, v16, vcc
	v_cmp_le_i32_e32 vcc, v37, v238
	v_or_b32_e32 v37, 57, v2
	s_nop 0
	v_cndmask_b32_e32 v33, v227, v33, vcc
	v_cmp_le_i32_e32 vcc, v37, v238
	v_or_b32_e32 v37, 26, v2
	s_nop 0
	v_cndmask_b32_e32 v17, v227, v17, vcc
	v_cmp_le_i32_e32 vcc, v37, v238
	v_or_b32_e32 v37, 58, v2
	s_nop 0
	v_cndmask_b32_e32 v34, v227, v34, vcc
	v_cmp_le_i32_e32 vcc, v37, v238
	v_or_b32_e32 v37, 27, v2
	v_or_b32_e32 v2, 59, v2
	v_cndmask_b32_e32 v18, v227, v18, vcc
	v_cmp_le_i32_e32 vcc, v37, v238
	s_nop 1
	v_cndmask_b32_e32 v35, v227, v35, vcc
	v_cmp_le_i32_e32 vcc, v2, v238
	s_nop 1
	v_cndmask_b32_e32 v19, v227, v19, vcc

.LBB0_264:
	s_waitcnt vmcnt(0) lgkmcnt(0)
	s_barrier
	v_lshl_add_u64 v[38:39], v[216:217], 0, s[30:31]
	s_mov_b32 m0, s76
	s_nop 0
	global_load_lds_dwordx4 v[38:39], off
	s_cmp_lg_u32 0, -1
	v_max3_f32 v2, v20, v21, v4
	s_cselect_b32 s1, 0, 0
	v_max3_f32 v37, v22, v23, v5
	v_max3_f32 v2, v2, v6, v7
	s_add_i32 s3, s1, s0
	v_max3_f32 v2, v2, v24, v25
	v_max3_f32 v37, v37, v26, v27
	v_lshl_add_u64 v[38:39], v[218:219], 0, s[28:29]
	s_add_i32 s0, s3, 0xe000
	s_mov_b32 m0, s0
	s_nop 0
	global_load_lds_dwordx4 v[38:39], off
	v_max3_f32 v2, v2, v8, v9
	v_max3_f32 v37, v37, v10, v11
	s_mov_b64 s[0:1], 0x90080
	v_max3_f32 v2, v2, v28, v29
	v_max3_f32 v37, v37, v30, v31
	v_lshl_add_u64 v[38:39], v[218:219], 0, s[0:1]
	s_add_i32 s3, s3, 0x10000
	s_mov_b32 m0, s3
	s_nop 0
	global_load_lds_dwordx4 v[38:39], off
	v_max3_f32 v2, v2, v12, v13
	v_max3_f32 v37, v37, v14, v15
	ds_read_b128 v[170:173], v240 offset:8192
	ds_read_b128 v[162:165], v240 offset:8704
	ds_read_b128 v[174:177], v240 offset:10240
	ds_read_b128 v[166:169], v240 offset:10752
	ds_read_b128 v[182:185], v240 offset:12288
	ds_read_b128 v[178:181], v240 offset:12800
	ds_read_b128 v[190:193], v240 offset:14336
	ds_read_b128 v[186:189], v240 offset:14848
	v_max3_f32 v2, v2, v32, v33
	v_max3_f32 v37, v37, v34, v35
	s_waitcnt vmcnt(3) lgkmcnt(0)
	s_barrier
	s_cmp_gt_i32 s85, 8
	v_max3_f32 v2, v2, v16, v17
	v_max3_f32 v37, v37, v18, v19
	s_mov_b64 s[0:1], -1
	v_max_f32_e32 v2, v2, v37
	s_nop 0
	v_mov_b32_e32 v37, v2
	s_nop 1
	v_permlane32_swap_b32_e32 v2, v37
	v_max_f32_e32 v2, v2, v37
	s_nop 0
	v_sub_f32_e32 v20, v20, v2
	v_sub_f32_e32 v37, v4, v2
	v_sub_f32_e32 v4, v21, v2
	v_sub_f32_e32 v21, v5, v2
	v_sub_f32_e32 v5, v22, v2
	v_sub_f32_e32 v22, v6, v2
	v_sub_f32_e32 v6, v23, v2
	v_sub_f32_e32 v23, v7, v2
	v_sub_f32_e32 v7, v24, v2
	v_sub_f32_e32 v24, v8, v2
	v_sub_f32_e32 v8, v25, v2
	v_sub_f32_e32 v25, v9, v2
	v_sub_f32_e32 v9, v26, v2
	v_sub_f32_e32 v26, v10, v2
	v_sub_f32_e32 v10, v27, v2
	v_sub_f32_e32 v27, v11, v2
	v_sub_f32_e32 v11, v28, v2
	v_sub_f32_e32 v28, v12, v2
	v_sub_f32_e32 v12, v29, v2
	v_sub_f32_e32 v29, v13, v2
	v_sub_f32_e32 v13, v30, v2
	v_sub_f32_e32 v30, v14, v2
	v_sub_f32_e32 v14, v31, v2
	v_sub_f32_e32 v31, v15, v2
	v_sub_f32_e32 v15, v32, v2
	v_sub_f32_e32 v32, v16, v2
	v_sub_f32_e32 v16, v33, v2
	v_sub_f32_e32 v33, v17, v2
	v_sub_f32_e32 v17, v34, v2
	v_sub_f32_e32 v34, v18, v2
	v_sub_f32_e32 v18, v35, v2
	v_add_f32_e32 v241, v3, v2
	v_sub_f32_e32 v35, v19, v2
	s_nop 0
	v_exp_f32_e32 v2, v20
	v_exp_f32_e32 v4, v4
	v_exp_f32_e32 v5, v5
	v_exp_f32_e32 v6, v6
	v_exp_f32_e32 v7, v7
	v_exp_f32_e32 v8, v8
	v_exp_f32_e32 v9, v9
	v_exp_f32_e32 v10, v10
	v_exp_f32_e32 v11, v11
	v_exp_f32_e32 v12, v12
	v_exp_f32_e32 v13, v13
	v_exp_f32_e32 v14, v14
	v_exp_f32_e32 v15, v15
	v_exp_f32_e32 v16, v16
	v_exp_f32_e32 v17, v17
	v_exp_f32_e32 v18, v18
	v_exp_f32_e32 v19, v37
	v_exp_f32_e32 v20, v21
	v_exp_f32_e32 v21, v22
	v_exp_f32_e32 v22, v23
	v_exp_f32_e32 v23, v24
	v_exp_f32_e32 v24, v25
	v_exp_f32_e32 v25, v26
	v_exp_f32_e32 v26, v27
	v_exp_f32_e32 v27, v28
	v_exp_f32_e32 v28, v29
	v_exp_f32_e32 v29, v30
	v_exp_f32_e32 v30, v31
	v_exp_f32_e32 v31, v32
	v_exp_f32_e32 v32, v33
	v_exp_f32_e32 v33, v34
	v_exp_f32_e32 v34, v35
	v_xor_b32_e32 v97, 0x80000000, v241
	v_cvt_pk_bf16_f32 v138, v2, v4
	v_cvt_pk_bf16_f32 v139, v5, v6
	v_cvt_pk_bf16_f32 v140, v7, v8
	v_cvt_pk_bf16_f32 v141, v9, v10
	v_cvt_pk_bf16_f32 v134, v11, v12
	v_cvt_pk_bf16_f32 v135, v13, v14
	v_cvt_pk_bf16_f32 v136, v15, v16
	v_cvt_pk_bf16_f32 v137, v17, v18
	v_cvt_pk_bf16_f32 v130, v19, v20
	v_cvt_pk_bf16_f32 v131, v21, v22
	v_cvt_pk_bf16_f32 v132, v23, v24
	v_cvt_pk_bf16_f32 v133, v25, v26
	v_cvt_pk_bf16_f32 v158, v27, v28
	v_cvt_pk_bf16_f32 v159, v29, v30
	v_cvt_pk_bf16_f32 v160, v31, v32
	v_cvt_pk_bf16_f32 v161, v33, v34
	s_cbranch_scc1 .LBB0_266
	v_mov_b32_e32 v96, v97
	v_mov_b32_e32 v82, v97
	v_mov_b32_e32 v83, v97
	v_mov_b32_e32 v84, v97
	v_mov_b32_e32 v85, v97
	v_mov_b32_e32 v86, v97
	v_mov_b32_e32 v87, v97
	v_mov_b32_e32 v88, v97
	v_mov_b32_e32 v89, v97
	v_mov_b32_e32 v90, v97
	v_mov_b32_e32 v91, v97
	v_mov_b32_e32 v92, v97
	v_mov_b32_e32 v93, v97
	v_mov_b32_e32 v94, v97
	v_mov_b32_e32 v95, v97
	v_mov_b64_e32 v[114:115], v[96:97]
	s_mov_b64 s[0:1], 0
	v_mov_b64_e32 v[112:113], v[94:95]
	v_mov_b64_e32 v[110:111], v[92:93]
	v_mov_b64_e32 v[108:109], v[90:91]
	v_mov_b64_e32 v[106:107], v[88:89]
	v_mov_b64_e32 v[104:105], v[86:87]
	v_mov_b64_e32 v[102:103], v[84:85]
	v_mov_b64_e32 v[100:101], v[82:83]

.LBB0_269:
	v_add_u32_e32 v2, s33, v242
	ds_read_b64_tr_b16 v[202:203], v2 offset:24576
	ds_read_b64_tr_b16 v[204:205], v2 offset:25088
	s_waitcnt lgkmcnt(9)
	v_mfma_f32_32x32x16_bf16 v[114:129], v[170:173], v[154:157], v[82:97]
	ds_read_b64_tr_b16 v[198:199], v2 offset:28672
	ds_read_b64_tr_b16 v[200:201], v2 offset:29184
	s_waitcnt lgkmcnt(10)
	v_mfma_f32_32x32x16_bf16 v[98:113], v[162:165], v[154:157], v[82:97]
	ds_read_b64_tr_b16 v[194:195], v2 offset:25600
	ds_read_b64_tr_b16 v[196:197], v2 offset:26112
	s_waitcnt lgkmcnt(11)
	v_mfma_f32_32x32x16_bf16 v[114:129], v[174:177], v[150:153], v[114:129]
	ds_read_b64_tr_b16 v[170:171], v2 offset:29696
	ds_read_b64_tr_b16 v[172:173], v2 offset:30208
	s_waitcnt lgkmcnt(12)
	v_mfma_f32_32x32x16_bf16 v[98:113], v[166:169], v[150:153], v[98:113]
	ds_read_b64_tr_b16 v[162:163], v2 offset:26624
	ds_read_b64_tr_b16 v[164:165], v2 offset:27136
	s_waitcnt lgkmcnt(13)
	v_mfma_f32_32x32x16_bf16 v[114:129], v[182:185], v[146:149], v[114:129]
	ds_read_b64_tr_b16 v[12:13], v2 offset:30720
	ds_read_b64_tr_b16 v[14:15], v2 offset:31232
	s_waitcnt lgkmcnt(14)
	v_mfma_f32_32x32x16_bf16 v[98:113], v[178:181], v[146:149], v[98:113]
	ds_read_b64_tr_b16 v[8:9], v2 offset:27648
	ds_read_b64_tr_b16 v[10:11], v2 offset:28160
	s_waitcnt lgkmcnt(14)
	v_mfma_f32_32x32x16_bf16 v[114:129], v[190:193], v[142:145], v[114:129]
	ds_read_b64_tr_b16 v[4:5], v2 offset:31744
	ds_read_b64_tr_b16 v[6:7], v2 offset:32256
	v_mfma_f32_32x32x16_bf16 v[98:113], v[186:189], v[142:145], v[98:113]
	s_mov_b32 s0, 0xfffb8000
	s_mov_b32 s1, -1
	v_lshl_add_u64 v[16:17], v[206:207], 0, s[0:1]
	s_add_i32 s0, s75, s76
	s_mov_b32 m0, s0
	s_nop 0
	global_load_lds_dwordx4 v[16:17], off
	s_nop 4
	v_max_f32_e32 v16, v115, v114
	v_max3_f32 v17, v116, v117, v99
	v_max3_f32 v16, v16, v98, v100
	v_max3_f32 v16, v16, v101, v118
	v_max3_f32 v17, v17, v120, v121
	v_max3_f32 v16, v16, v119, v102
	v_max3_f32 v17, v17, v104, v105
	v_max3_f32 v16, v16, v103, v122
	v_max3_f32 v17, v17, v124, v125
	v_max3_f32 v16, v16, v123, v106
	v_max3_f32 v17, v17, v108, v109
	v_max3_f32 v16, v16, v107, v126
	v_max3_f32 v17, v17, v128, v129
	v_max3_f32 v16, v16, v127, v110
	v_max3_f32 v17, v17, v112, v113
	v_max3_f32 v16, v16, v111, v17
	v_mov_b32_e32 v17, v16
	s_nop 1
	v_permlane32_swap_b32_e32 v16, v17
	s_add_i32 s0, s86, s77
	s_mov_b32 m0, s0
	s_nop 0
	global_load_lds_dwordx4 v[210:211], off
	v_max_f32_e32 v16, v16, v17
	s_addk_i32 s0, 0x2000
	s_mov_b32 m0, s0
	s_nop 0
	global_load_lds_dwordx4 v[208:209], off
	v_cmp_lt_f32_e32 vcc, s79, v16
	s_cmp_lg_u64 vcc, 0
	s_cselect_b64 s[0:1], -1, 0
	s_cbranch_vccnz .LBB0_275
.LBB0_270:
	s_waitcnt lgkmcnt(14)
	v_mfma_f32_32x32x16_bf16 v[66:81], v[138:141], v[202:205], v[66:81]
	v_exp_f32_e32 v114, v114
	v_exp_f32_e32 v115, v115
	v_exp_f32_e32 v116, v116
	v_exp_f32_e32 v117, v117
	ds_read_b64_tr_b16 v[166:167], v2 offset:32768
	ds_read_b64_tr_b16 v[168:169], v2 offset:33280
	s_waitcnt lgkmcnt(14)
	v_mfma_f32_32x32x16_bf16 v[50:65], v[138:141], v[198:201], v[50:65]
	v_exp_f32_e32 v118, v118
	v_exp_f32_e32 v119, v119
	v_exp_f32_e32 v120, v120
	v_exp_f32_e32 v121, v121
	ds_read_b64_tr_b16 v[174:175], v2 offset:36864
	ds_read_b64_tr_b16 v[176:177], v2 offset:37376
	s_waitcnt lgkmcnt(14)
	v_mfma_f32_32x32x16_bf16 v[66:81], v[134:137], v[194:197], v[66:81]
	v_exp_f32_e32 v122, v122
	v_exp_f32_e32 v123, v123
	v_exp_f32_e32 v124, v124
	v_exp_f32_e32 v125, v125
	ds_read_b64_tr_b16 v[178:179], v2 offset:33792
	ds_read_b64_tr_b16 v[180:181], v2 offset:34304
	s_waitcnt lgkmcnt(14)
	v_mfma_f32_32x32x16_bf16 v[50:65], v[134:137], v[170:173], v[50:65]
	v_exp_f32_e32 v126, v126
	v_exp_f32_e32 v127, v127
	v_exp_f32_e32 v128, v128
	v_exp_f32_e32 v129, v129
	ds_read_b64_tr_b16 v[182:183], v2 offset:37888
	ds_read_b64_tr_b16 v[184:185], v2 offset:38400
	s_waitcnt lgkmcnt(14)
	v_mfma_f32_32x32x16_bf16 v[66:81], v[130:133], v[162:165], v[66:81]
	v_exp_f32_e32 v98, v98
	v_exp_f32_e32 v99, v99
	v_exp_f32_e32 v100, v100
	v_exp_f32_e32 v101, v101
	ds_read_b64_tr_b16 v[186:187], v2 offset:34816
	ds_read_b64_tr_b16 v[188:189], v2 offset:35328
	s_waitcnt lgkmcnt(14)
	v_mfma_f32_32x32x16_bf16 v[50:65], v[130:133], v[12:15], v[50:65]
	v_exp_f32_e32 v102, v102
	v_exp_f32_e32 v103, v103
	v_exp_f32_e32 v104, v104
	v_exp_f32_e32 v105, v105
	ds_read_b64_tr_b16 v[190:191], v2 offset:38912
	ds_read_b64_tr_b16 v[192:193], v2 offset:39424
	s_waitcnt lgkmcnt(14)
	v_mfma_f32_32x32x16_bf16 v[66:81], v[158:161], v[8:11], v[66:81]
	v_exp_f32_e32 v106, v106
	v_exp_f32_e32 v107, v107
	v_exp_f32_e32 v108, v108
	v_exp_f32_e32 v109, v109
	ds_read_b64_tr_b16 v[194:195], v2 offset:35840
	ds_read_b64_tr_b16 v[196:197], v2 offset:36352
	s_waitcnt lgkmcnt(14)
	v_mfma_f32_32x32x16_bf16 v[50:65], v[158:161], v[4:7], v[50:65]
	v_exp_f32_e32 v110, v110
	v_exp_f32_e32 v111, v111
	v_exp_f32_e32 v112, v112
	v_exp_f32_e32 v113, v113
	ds_read_b64_tr_b16 v[4:5], v2 offset:39936
	ds_read_b64_tr_b16 v[6:7], v2 offset:40448
	v_add_f32_e32 v2, v114, v115
	s_waitcnt lgkmcnt(14)
	v_mfma_f32_32x32x16_bf16 v[34:49], v[138:141], v[166:169], v[34:49]
	v_add_f32_e32 v2, v116, v2
	v_add_f32_e32 v2, v117, v2
	v_add_f32_e32 v2, v118, v2
	v_add_f32_e32 v2, v119, v2
	v_add_u32_e32 v16, s88, v240
	ds_read_b128 v[12:15], v16
	ds_read_b128 v[8:11], v16 offset:512
	s_waitcnt lgkmcnt(14)
	v_mfma_f32_32x32x16_bf16 v[18:33], v[138:141], v[174:177], v[18:33]
	v_add_f32_e32 v2, v120, v2
	v_add_f32_e32 v2, v121, v2
	v_add_f32_e32 v2, v122, v2
	v_add_f32_e32 v2, v123, v2
	ds_read_b128 v[166:169], v16 offset:2048
	ds_read_b128 v[162:165], v16 offset:2560
	s_waitcnt lgkmcnt(14)
	v_mfma_f32_32x32x16_bf16 v[34:49], v[134:137], v[178:181], v[34:49]
	v_add_f32_e32 v2, v124, v2
	v_add_f32_e32 v2, v125, v2
	v_add_f32_e32 v2, v126, v2
	v_add_f32_e32 v2, v127, v2
	v_cvt_pk_bf16_f32 v138, v114, v115
	v_cvt_pk_bf16_f32 v139, v116, v117
	ds_read_b128 v[174:177], v16 offset:4096
	ds_read_b128 v[170:173], v16 offset:4608
	s_waitcnt lgkmcnt(14)
	v_mfma_f32_32x32x16_bf16 v[18:33], v[134:137], v[182:185], v[18:33]
	v_add_f32_e32 v2, v128, v2
	v_add_f32_e32 v2, v129, v2
	v_add_f32_e32 v2, v98, v2
	v_add_f32_e32 v2, v99, v2
	v_cvt_pk_bf16_f32 v140, v118, v119
	v_cvt_pk_bf16_f32 v141, v120, v121
	ds_read_b128 v[182:185], v16 offset:6144
	ds_read_b128 v[178:181], v16 offset:6656
	s_waitcnt lgkmcnt(14)
	v_mfma_f32_32x32x16_bf16 v[34:49], v[130:133], v[186:189], v[34:49]
	v_add_f32_e32 v2, v100, v2
	v_add_f32_e32 v2, v101, v2
	v_add_f32_e32 v2, v102, v2
	v_add_f32_e32 v2, v103, v2
	v_cvt_pk_bf16_f32 v134, v122, v123
	v_cvt_pk_bf16_f32 v135, v124, v125
	s_waitcnt lgkmcnt(12)
	v_mfma_f32_32x32x16_bf16 v[18:33], v[130:133], v[190:193], v[18:33]
	v_add_f32_e32 v2, v104, v2
	v_add_f32_e32 v2, v105, v2
	v_add_f32_e32 v2, v106, v2
	v_add_f32_e32 v2, v107, v2
	v_cvt_pk_bf16_f32 v136, v126, v127
	v_cvt_pk_bf16_f32 v137, v128, v129
	s_waitcnt lgkmcnt(10)
	v_mfma_f32_32x32x16_bf16 v[34:49], v[158:161], v[194:197], v[34:49]
	v_add_f32_e32 v2, v108, v2
	v_add_f32_e32 v2, v109, v2
	v_add_f32_e32 v2, v110, v2
	v_add_f32_e32 v2, v111, v2
	v_cvt_pk_bf16_f32 v130, v98, v99
	v_cvt_pk_bf16_f32 v131, v100, v101
	s_waitcnt lgkmcnt(8)
	v_mfma_f32_32x32x16_bf16 v[18:33], v[158:161], v[4:7], v[18:33]
	v_add_f32_e32 v2, v112, v2
	v_add_f32_e32 v2, v113, v2
	v_cvt_pk_bf16_f32 v132, v102, v103
	v_cvt_pk_bf16_f32 v133, v104, v105
	v_cvt_pk_bf16_f32 v4, v106, v107
	v_cvt_pk_bf16_f32 v5, v108, v109
	v_cvt_pk_bf16_f32 v6, v110, v111
	v_cvt_pk_bf16_f32 v7, v112, v113
	s_waitcnt vmcnt(3) lgkmcnt(0)
	s_barrier
	s_andn2_b64 vcc, exec, s[0:1]
	s_cbranch_vccnz .LBB0_272
	s_waitcnt lgkmcnt(0)
	ds_read2_b32 v[16:17], v234 offset1:1
	ds_read2_b32 v[98:99], v234 offset0:2 offset1:3
	ds_read2_b32 v[100:101], v234 offset0:8 offset1:9
	ds_read2_b32 v[102:103], v234 offset0:10 offset1:11
	s_waitcnt lgkmcnt(3)
	v_mul_f32_e32 v66, v66, v16
	v_mul_f32_e32 v50, v50, v16
	v_mul_f32_e32 v34, v34, v16
	v_mul_f32_e32 v18, v18, v16
	v_mul_f32_e32 v67, v67, v17
	v_mul_f32_e32 v51, v51, v17
	v_mul_f32_e32 v35, v35, v17
	v_mul_f32_e32 v19, v19, v17
	s_waitcnt lgkmcnt(2)
	v_mul_f32_e32 v68, v68, v98
	v_mul_f32_e32 v52, v52, v98
	v_mul_f32_e32 v36, v36, v98
	v_mul_f32_e32 v20, v20, v98
	v_mul_f32_e32 v69, v69, v99
	v_mul_f32_e32 v53, v53, v99
	v_mul_f32_e32 v37, v37, v99
	v_mul_f32_e32 v21, v21, v99
	s_waitcnt lgkmcnt(1)
	v_mul_f32_e32 v70, v70, v100
	v_mul_f32_e32 v54, v54, v100
	v_mul_f32_e32 v38, v38, v100
	v_mul_f32_e32 v22, v22, v100
	v_mul_f32_e32 v71, v71, v101
	v_mul_f32_e32 v55, v55, v101
	v_mul_f32_e32 v39, v39, v101
	v_mul_f32_e32 v23, v23, v101
	s_waitcnt lgkmcnt(0)
	v_mul_f32_e32 v72, v72, v102
	v_mul_f32_e32 v56, v56, v102
	v_mul_f32_e32 v40, v40, v102
	v_mul_f32_e32 v24, v24, v102
	v_mul_f32_e32 v73, v73, v103
	v_mul_f32_e32 v57, v57, v103
	v_mul_f32_e32 v41, v41, v103
	ds_read2_b32 v[16:17], v234 offset0:16 offset1:17
	v_mul_f32_e32 v25, v25, v103
	ds_read2_b32 v[98:99], v234 offset0:18 offset1:19
	ds_read2_b32 v[100:101], v234 offset0:24 offset1:25
	ds_read2_b32 v[102:103], v234 offset0:26 offset1:27
	s_waitcnt lgkmcnt(3)
	v_mul_f32_e32 v74, v74, v16
	v_mul_f32_e32 v58, v58, v16
	v_mul_f32_e32 v42, v42, v16
	v_mul_f32_e32 v26, v26, v16
	v_mul_f32_e32 v75, v75, v17
	v_mul_f32_e32 v59, v59, v17
	v_mul_f32_e32 v43, v43, v17
	v_mul_f32_e32 v27, v27, v17
	s_waitcnt lgkmcnt(2)
	v_mul_f32_e32 v76, v76, v98
	v_mul_f32_e32 v60, v60, v98
	v_mul_f32_e32 v44, v44, v98
	v_mul_f32_e32 v28, v28, v98
	v_mul_f32_e32 v77, v77, v99
	v_mul_f32_e32 v61, v61, v99
	v_mul_f32_e32 v45, v45, v99
	v_mul_f32_e32 v29, v29, v99
	s_waitcnt lgkmcnt(1)
	v_mul_f32_e32 v78, v78, v100
	v_mul_f32_e32 v62, v62, v100
	v_mul_f32_e32 v46, v46, v100
	v_mul_f32_e32 v30, v30, v100
	v_mul_f32_e32 v79, v79, v101
	v_mul_f32_e32 v63, v63, v101
	v_mul_f32_e32 v47, v47, v101
	v_mul_f32_e32 v31, v31, v101
	s_waitcnt lgkmcnt(0)
	v_mul_f32_e32 v80, v80, v102
	v_mul_f32_e32 v64, v64, v102
	v_mul_f32_e32 v48, v48, v102
	v_mul_f32_e32 v32, v32, v102
	v_mul_f32_e32 v81, v81, v103
	v_mul_f32_e32 v65, v65, v103
	v_mul_f32_e32 v49, v49, v103
	v_mul_f32_e32 v33, v33, v103
.LBB0_272:
	s_add_i32 s0, s33, 0x4000
	s_add_i32 s1, s86, 0x4000
	v_add_f32_e32 v2, v243, v2
	s_and_b32 s0, s0, 0xffff
	s_and_b32 s1, s1, 0xffff
	v_add_u32_e32 v16, s0, v242
	ds_read_b64_tr_b16 v[194:195], v16 offset:24576
	ds_read_b64_tr_b16 v[196:197], v16 offset:25088
	s_waitcnt lgkmcnt(9)
	v_mfma_f32_32x32x16_bf16 v[114:129], v[12:15], v[154:157], v[82:97]
	ds_read_b64_tr_b16 v[190:191], v16 offset:28672
	ds_read_b64_tr_b16 v[192:193], v16 offset:29184
	s_waitcnt lgkmcnt(10)
	v_mfma_f32_32x32x16_bf16 v[98:113], v[8:11], v[154:157], v[82:97]
	ds_read_b64_tr_b16 v[186:187], v16 offset:25600
	ds_read_b64_tr_b16 v[188:189], v16 offset:26112
	s_waitcnt lgkmcnt(11)
	v_mfma_f32_32x32x16_bf16 v[114:129], v[166:169], v[150:153], v[114:129]
	ds_read_b64_tr_b16 v[166:167], v16 offset:29696
	ds_read_b64_tr_b16 v[168:169], v16 offset:30208
	s_waitcnt lgkmcnt(12)
	v_mfma_f32_32x32x16_bf16 v[98:113], v[162:165], v[150:153], v[98:113]
	ds_read_b64_tr_b16 v[162:163], v16 offset:26624
	ds_read_b64_tr_b16 v[164:165], v16 offset:27136
	s_waitcnt lgkmcnt(13)
	v_mfma_f32_32x32x16_bf16 v[114:129], v[174:177], v[146:149], v[114:129]
	ds_read_b64_tr_b16 v[158:159], v16 offset:30720
	ds_read_b64_tr_b16 v[160:161], v16 offset:31232
	s_waitcnt lgkmcnt(14)
	v_mfma_f32_32x32x16_bf16 v[98:113], v[170:173], v[146:149], v[98:113]
	ds_read_b64_tr_b16 v[12:13], v16 offset:27648
	ds_read_b64_tr_b16 v[14:15], v16 offset:28160
	s_waitcnt lgkmcnt(14)
	v_mfma_f32_32x32x16_bf16 v[114:129], v[182:185], v[142:145], v[114:129]
	ds_read_b64_tr_b16 v[8:9], v16 offset:31744
	ds_read_b64_tr_b16 v[10:11], v16 offset:32256
	v_mfma_f32_32x32x16_bf16 v[98:113], v[178:181], v[142:145], v[98:113]
	s_add_i32 s0, s88, s76
	s_mov_b32 m0, s0
	s_nop 0
	global_load_lds_dwordx4 v[206:207], off
	v_lshl_add_u64 v[170:171], v[210:211], 0, s[26:27]
	s_add_i32 s0, s1, s77
	s_mov_b32 m0, s0
	s_nop 0
	global_load_lds_dwordx4 v[170:171], off
	v_lshl_add_u64 v[170:171], v[208:209], 0, s[26:27]
	s_addk_i32 s0, 0x2000
	s_mov_b32 m0, s0
	s_nop 0
	global_load_lds_dwordx4 v[170:171], off
	s_nop 3
	v_max_f32_e32 v17, v115, v114
	v_max3_f32 v170, v116, v117, v99
	v_max3_f32 v17, v17, v98, v100
	v_max3_f32 v17, v17, v101, v118
	v_max3_f32 v170, v170, v120, v121
	v_max3_f32 v17, v17, v119, v102
	v_max3_f32 v170, v170, v104, v105
	v_max3_f32 v17, v17, v103, v122
	v_max3_f32 v170, v170, v124, v125
	v_max3_f32 v17, v17, v123, v106
	v_max3_f32 v170, v170, v108, v109
	v_max3_f32 v17, v17, v107, v126
	v_max3_f32 v170, v170, v128, v129
	v_max3_f32 v17, v17, v127, v110
	v_max3_f32 v170, v170, v112, v113
	v_max3_f32 v17, v17, v111, v170
	v_mov_b32_e32 v170, v17
	s_nop 1
	v_permlane32_swap_b32_e32 v17, v170
	v_max_f32_e32 v17, v17, v170
	v_cmp_lt_f32_e32 vcc, s79, v17
	s_cmp_lg_u64 vcc, 0
	s_cselect_b64 s[0:1], -1, 0
	s_cbranch_vccnz .LBB0_278
.LBB0_273:
	s_add_i32 s36, s88, 0x2000
	s_cmpk_lg_i32 s88, 0x4000
	s_cselect_b32 s75, s36, 0
	s_waitcnt lgkmcnt(14)
	v_mfma_f32_32x32x16_bf16 v[66:81], v[138:141], v[194:197], v[66:81]
	v_exp_f32_e32 v114, v114
	v_exp_f32_e32 v115, v115
	v_exp_f32_e32 v116, v116
	v_exp_f32_e32 v117, v117
	ds_read_b64_tr_b16 v[170:171], v16 offset:32768
	ds_read_b64_tr_b16 v[172:173], v16 offset:33280
	s_waitcnt lgkmcnt(14)
	v_mfma_f32_32x32x16_bf16 v[50:65], v[138:141], v[190:193], v[50:65]
	v_exp_f32_e32 v118, v118
	v_exp_f32_e32 v119, v119
	v_exp_f32_e32 v120, v120
	v_exp_f32_e32 v121, v121
	ds_read_b64_tr_b16 v[174:175], v16 offset:36864
	ds_read_b64_tr_b16 v[176:177], v16 offset:37376
	s_waitcnt lgkmcnt(14)
	v_mfma_f32_32x32x16_bf16 v[66:81], v[134:137], v[186:189], v[66:81]
	v_exp_f32_e32 v122, v122
	v_exp_f32_e32 v123, v123
	v_exp_f32_e32 v124, v124
	v_exp_f32_e32 v125, v125
	ds_read_b64_tr_b16 v[178:179], v16 offset:33792
	ds_read_b64_tr_b16 v[180:181], v16 offset:34304
	s_waitcnt lgkmcnt(14)
	v_mfma_f32_32x32x16_bf16 v[50:65], v[134:137], v[166:169], v[50:65]
	v_exp_f32_e32 v126, v126
	v_exp_f32_e32 v127, v127
	v_exp_f32_e32 v128, v128
	v_exp_f32_e32 v129, v129
	ds_read_b64_tr_b16 v[186:187], v16 offset:37888
	ds_read_b64_tr_b16 v[188:189], v16 offset:38400
	s_waitcnt lgkmcnt(14)
	v_mfma_f32_32x32x16_bf16 v[66:81], v[130:133], v[162:165], v[66:81]
	v_exp_f32_e32 v98, v98
	v_exp_f32_e32 v99, v99
	v_exp_f32_e32 v100, v100
	v_exp_f32_e32 v101, v101
	ds_read_b64_tr_b16 v[194:195], v16 offset:34816
	ds_read_b64_tr_b16 v[196:197], v16 offset:35328
	s_waitcnt lgkmcnt(14)
	v_mfma_f32_32x32x16_bf16 v[50:65], v[130:133], v[158:161], v[50:65]
	v_exp_f32_e32 v102, v102
	v_exp_f32_e32 v103, v103
	v_exp_f32_e32 v104, v104
	v_exp_f32_e32 v105, v105
	ds_read_b64_tr_b16 v[158:159], v16 offset:38912
	ds_read_b64_tr_b16 v[160:161], v16 offset:39424
	s_waitcnt lgkmcnt(14)
	v_mfma_f32_32x32x16_bf16 v[66:81], v[4:7], v[12:15], v[66:81]
	v_exp_f32_e32 v106, v106
	v_exp_f32_e32 v107, v107
	v_exp_f32_e32 v108, v108
	v_exp_f32_e32 v109, v109
	ds_read_b64_tr_b16 v[12:13], v16 offset:35840
	ds_read_b64_tr_b16 v[14:15], v16 offset:36352
	s_waitcnt lgkmcnt(14)
	v_mfma_f32_32x32x16_bf16 v[50:65], v[4:7], v[8:11], v[50:65]
	v_exp_f32_e32 v110, v110
	v_exp_f32_e32 v111, v111
	v_exp_f32_e32 v112, v112
	v_exp_f32_e32 v113, v113
	ds_read_b64_tr_b16 v[198:199], v16 offset:39936
	ds_read_b64_tr_b16 v[200:201], v16 offset:40448
	v_add_f32_e32 v8, v114, v115
	s_waitcnt lgkmcnt(14)
	v_mfma_f32_32x32x16_bf16 v[34:49], v[138:141], v[170:173], v[34:49]
	v_add_f32_e32 v8, v116, v8
	v_add_f32_e32 v8, v117, v8
	v_add_f32_e32 v8, v118, v8
	v_add_f32_e32 v8, v119, v8
	v_add_u32_e32 v9, s75, v240
	ds_read_b128 v[170:173], v9
	ds_read_b128 v[162:165], v9 offset:512
	s_waitcnt lgkmcnt(14)
	v_mfma_f32_32x32x16_bf16 v[18:33], v[138:141], v[174:177], v[18:33]
	v_add_f32_e32 v8, v120, v8
	v_add_f32_e32 v8, v121, v8
	v_add_f32_e32 v8, v122, v8
	v_add_f32_e32 v8, v123, v8
	ds_read_b128 v[174:177], v9 offset:2048
	ds_read_b128 v[166:169], v9 offset:2560
	s_waitcnt lgkmcnt(14)
	v_mfma_f32_32x32x16_bf16 v[34:49], v[134:137], v[178:181], v[34:49]
	v_add_f32_e32 v8, v124, v8
	v_add_f32_e32 v8, v125, v8
	v_add_f32_e32 v8, v126, v8
	v_add_f32_e32 v8, v127, v8
	v_cvt_pk_bf16_f32 v138, v114, v115
	v_cvt_pk_bf16_f32 v139, v116, v117
	ds_read_b128 v[182:185], v9 offset:4096
	ds_read_b128 v[178:181], v9 offset:4608
	s_waitcnt lgkmcnt(14)
	v_mfma_f32_32x32x16_bf16 v[18:33], v[134:137], v[186:189], v[18:33]
	v_add_f32_e32 v8, v128, v8
	v_add_f32_e32 v8, v129, v8
	v_add_f32_e32 v8, v98, v8
	v_add_f32_e32 v8, v99, v8
	v_cvt_pk_bf16_f32 v140, v118, v119
	v_cvt_pk_bf16_f32 v141, v120, v121
	ds_read_b128 v[190:193], v9 offset:6144
	ds_read_b128 v[186:189], v9 offset:6656
	s_waitcnt lgkmcnt(14)
	v_mfma_f32_32x32x16_bf16 v[34:49], v[130:133], v[194:197], v[34:49]
	v_add_f32_e32 v8, v100, v8
	v_add_f32_e32 v8, v101, v8
	v_add_f32_e32 v8, v102, v8
	v_add_f32_e32 v8, v103, v8
	v_cvt_pk_bf16_f32 v134, v122, v123
	v_cvt_pk_bf16_f32 v135, v124, v125
	s_waitcnt lgkmcnt(12)
	v_mfma_f32_32x32x16_bf16 v[18:33], v[130:133], v[158:161], v[18:33]
	v_add_f32_e32 v8, v104, v8
	v_add_f32_e32 v8, v105, v8
	v_add_f32_e32 v8, v106, v8
	v_add_f32_e32 v8, v107, v8
	v_cvt_pk_bf16_f32 v136, v126, v127
	v_cvt_pk_bf16_f32 v137, v128, v129
	s_waitcnt lgkmcnt(10)
	v_mfma_f32_32x32x16_bf16 v[34:49], v[4:7], v[12:15], v[34:49]
	v_add_f32_e32 v8, v108, v8
	v_add_f32_e32 v8, v109, v8
	v_add_f32_e32 v8, v110, v8
	v_add_f32_e32 v8, v111, v8
	v_cvt_pk_bf16_f32 v130, v98, v99
	v_cvt_pk_bf16_f32 v131, v100, v101
	s_waitcnt lgkmcnt(8)
	v_mfma_f32_32x32x16_bf16 v[18:33], v[4:7], v[198:201], v[18:33]
	v_add_f32_e32 v8, v112, v8
	v_add_f32_e32 v8, v113, v8
	v_cvt_pk_bf16_f32 v132, v102, v103
	v_cvt_pk_bf16_f32 v133, v104, v105
	v_cvt_pk_bf16_f32 v158, v106, v107
	v_cvt_pk_bf16_f32 v159, v108, v109
	v_cvt_pk_bf16_f32 v160, v110, v111
	v_cvt_pk_bf16_f32 v161, v112, v113
	s_waitcnt vmcnt(3) lgkmcnt(0)
	s_barrier
	s_andn2_b64 vcc, exec, s[0:1]
	s_cbranch_vccnz .LBB0_268
	s_waitcnt lgkmcnt(0)
	ds_read2_b32 v[4:5], v234 offset1:1
	ds_read2_b32 v[6:7], v234 offset0:2 offset1:3
	ds_read2_b32 v[10:11], v234 offset0:8 offset1:9
	ds_read2_b32 v[12:13], v234 offset0:10 offset1:11
	s_waitcnt lgkmcnt(3)
	v_mul_f32_e32 v66, v66, v4
	v_mul_f32_e32 v50, v50, v4
	v_mul_f32_e32 v34, v34, v4
	v_mul_f32_e32 v18, v18, v4
	v_mul_f32_e32 v67, v67, v5
	v_mul_f32_e32 v51, v51, v5
	v_mul_f32_e32 v35, v35, v5
	v_mul_f32_e32 v19, v19, v5
	s_waitcnt lgkmcnt(2)
	v_mul_f32_e32 v68, v68, v6
	v_mul_f32_e32 v52, v52, v6
	v_mul_f32_e32 v36, v36, v6
	v_mul_f32_e32 v20, v20, v6
	v_mul_f32_e32 v69, v69, v7
	v_mul_f32_e32 v53, v53, v7
	v_mul_f32_e32 v37, v37, v7
	v_mul_f32_e32 v21, v21, v7
	s_waitcnt lgkmcnt(1)
	v_mul_f32_e32 v70, v70, v10
	v_mul_f32_e32 v54, v54, v10
	v_mul_f32_e32 v38, v38, v10
	v_mul_f32_e32 v22, v22, v10
	v_mul_f32_e32 v71, v71, v11
	v_mul_f32_e32 v55, v55, v11
	v_mul_f32_e32 v39, v39, v11
	v_mul_f32_e32 v23, v23, v11
	s_waitcnt lgkmcnt(0)
	v_mul_f32_e32 v72, v72, v12
	v_mul_f32_e32 v56, v56, v12
	v_mul_f32_e32 v40, v40, v12
	v_mul_f32_e32 v24, v24, v12
	v_mul_f32_e32 v73, v73, v13
	v_mul_f32_e32 v57, v57, v13
	v_mul_f32_e32 v41, v41, v13
	ds_read2_b32 v[4:5], v234 offset0:16 offset1:17
	v_mul_f32_e32 v25, v25, v13
	ds_read2_b32 v[6:7], v234 offset0:18 offset1:19
	ds_read2_b32 v[10:11], v234 offset0:24 offset1:25
	ds_read2_b32 v[12:13], v234 offset0:26 offset1:27
	s_waitcnt lgkmcnt(3)
	v_mul_f32_e32 v74, v74, v4
	v_mul_f32_e32 v58, v58, v4
	v_mul_f32_e32 v42, v42, v4
	v_mul_f32_e32 v26, v26, v4
	v_mul_f32_e32 v75, v75, v5
	v_mul_f32_e32 v59, v59, v5
	v_mul_f32_e32 v43, v43, v5
	v_mul_f32_e32 v27, v27, v5
	s_waitcnt lgkmcnt(2)
	v_mul_f32_e32 v76, v76, v6
	v_mul_f32_e32 v60, v60, v6
	v_mul_f32_e32 v44, v44, v6
	v_mul_f32_e32 v28, v28, v6
	v_mul_f32_e32 v77, v77, v7
	v_mul_f32_e32 v61, v61, v7
	v_mul_f32_e32 v45, v45, v7
	v_mul_f32_e32 v29, v29, v7
	s_waitcnt lgkmcnt(1)
	v_mul_f32_e32 v78, v78, v10
	v_mul_f32_e32 v62, v62, v10
	v_mul_f32_e32 v46, v46, v10
	v_mul_f32_e32 v30, v30, v10
	v_mul_f32_e32 v79, v79, v11
	v_mul_f32_e32 v63, v63, v11
	v_mul_f32_e32 v47, v47, v11
	v_mul_f32_e32 v31, v31, v11
	s_waitcnt lgkmcnt(0)
	v_mul_f32_e32 v80, v80, v12
	v_mul_f32_e32 v64, v64, v12
	v_mul_f32_e32 v48, v48, v12
	v_mul_f32_e32 v32, v32, v12
	v_mul_f32_e32 v81, v81, v13
	v_mul_f32_e32 v65, v65, v13
	v_mul_f32_e32 v49, v49, v13
	v_mul_f32_e32 v33, v33, v13
	s_branch .LBB0_268

.LBB0_284:
	v_add_u32_e32 v206, s33, v242
	ds_read_b64_tr_b16 v[202:203], v206 offset:24576
	ds_read_b64_tr_b16 v[204:205], v206 offset:25088
	s_waitcnt lgkmcnt(9)
	v_mfma_f32_32x32x16_bf16 v[114:129], v[170:173], v[154:157], v[82:97]
	ds_read_b64_tr_b16 v[198:199], v206 offset:28672
	ds_read_b64_tr_b16 v[200:201], v206 offset:29184
	s_waitcnt lgkmcnt(10)
	v_mfma_f32_32x32x16_bf16 v[98:113], v[162:165], v[154:157], v[82:97]
	ds_read_b64_tr_b16 v[194:195], v206 offset:25600
	ds_read_b64_tr_b16 v[196:197], v206 offset:26112
	s_waitcnt lgkmcnt(11)
	v_mfma_f32_32x32x16_bf16 v[114:129], v[174:177], v[150:153], v[114:129]
	ds_read_b64_tr_b16 v[170:171], v206 offset:29696
	ds_read_b64_tr_b16 v[172:173], v206 offset:30208
	s_waitcnt lgkmcnt(12)
	v_mfma_f32_32x32x16_bf16 v[98:113], v[166:169], v[150:153], v[98:113]
	ds_read_b64_tr_b16 v[162:163], v206 offset:26624
	ds_read_b64_tr_b16 v[164:165], v206 offset:27136
	s_waitcnt lgkmcnt(13)
	v_mfma_f32_32x32x16_bf16 v[114:129], v[182:185], v[146:149], v[114:129]
	ds_read_b64_tr_b16 v[12:13], v206 offset:30720
	ds_read_b64_tr_b16 v[14:15], v206 offset:31232
	s_waitcnt lgkmcnt(14)
	v_mfma_f32_32x32x16_bf16 v[98:113], v[178:181], v[146:149], v[98:113]
	ds_read_b64_tr_b16 v[8:9], v206 offset:27648
	ds_read_b64_tr_b16 v[10:11], v206 offset:28160
	s_waitcnt lgkmcnt(14)
	v_mfma_f32_32x32x16_bf16 v[114:129], v[190:193], v[142:145], v[114:129]
	ds_read_b64_tr_b16 v[4:5], v206 offset:31744
	ds_read_b64_tr_b16 v[6:7], v206 offset:32256
	v_mfma_f32_32x32x16_bf16 v[98:113], v[186:189], v[142:145], v[98:113]
	s_add_i32 s38, s87, 3
	s_cmp_lt_i32 s38, s85
	s_cselect_b64 s[0:1], -1, 0
	s_cmp_ge_i32 s38, s85
	s_cselect_b64 s[42:43], -1, 0
	s_and_b64 vcc, exec, s[42:43]
	v_lshl_add_u64 v[16:17], v[216:217], 0, s[36:37]
	s_cbranch_vccnz .LBB0_286
	v_lshl_add_u64 v[166:167], v[16:17], 0, s[30:31]
	s_add_i32 s38, s75, s76
	s_mov_b32 m0, s38
	s_nop 0
	global_load_lds_dwordx4 v[166:167], off
.LBB0_286:
	s_add_i32 s74, s87, 2
	s_cmp_lt_i32 s74, s85
	s_cselect_b64 s[44:45], -1, 0
	s_cmp_ge_i32 s74, s85
	s_cselect_b64 s[46:47], -1, 0
	s_and_b64 vcc, exec, s[46:47]
	v_lshl_add_u64 v[224:225], v[218:219], 0, s[36:37]
	v_lshl_add_u64 v[222:223], v[220:221], 0, s[36:37]
	s_cbranch_vccnz .LBB0_288
	v_lshl_add_u64 v[166:167], v[224:225], 0, s[28:29]
	s_add_i32 s38, s86, s77
	s_mov_b32 m0, s38
	s_nop 0
	global_load_lds_dwordx4 v[166:167], off
	v_lshl_add_u64 v[166:167], v[222:223], 0, s[28:29]
	s_addk_i32 s38, 0x2000
	s_mov_b32 m0, s38
	s_nop 0
	global_load_lds_dwordx4 v[166:167], off

.LBB0_292:
	s_nop 0
	v_max_f32_e32 v166, v115, v114
	v_max3_f32 v167, v116, v117, v99
	v_max3_f32 v166, v166, v98, v100
	v_max3_f32 v166, v166, v101, v118
	v_max3_f32 v167, v167, v120, v121
	v_max3_f32 v166, v166, v119, v102
	v_max3_f32 v167, v167, v104, v105
	v_max3_f32 v166, v166, v103, v122
	v_max3_f32 v167, v167, v124, v125
	v_max3_f32 v166, v166, v123, v106
	v_max3_f32 v167, v167, v108, v109
	v_max3_f32 v166, v166, v107, v126
	v_max3_f32 v167, v167, v128, v129
	v_max3_f32 v166, v166, v127, v110
	v_max3_f32 v167, v167, v112, v113
	v_max3_f32 v166, v166, v111, v167
	v_mov_b32_e32 v167, v166
	s_nop 1
	v_permlane32_swap_b32_e32 v166, v167
	v_max_f32_e32 v166, v166, v167
	v_cmp_lt_f32_e32 vcc, s79, v166
	s_cmp_lg_u64 vcc, 0
	s_cselect_b64 s[50:51], -1, 0
	s_cbranch_vccnz .LBB0_332

.LBB0_301:
	s_add_i32 s38, s33, 0x4000
	s_and_b32 s38, s38, 0xffff
	v_add_u32_e32 v249, s38, v242
	ds_read_b64_tr_b16 v[210:211], v249 offset:24576
	ds_read_b64_tr_b16 v[212:213], v249 offset:25088
	s_waitcnt lgkmcnt(9)
	v_mfma_f32_32x32x16_bf16 v[114:129], v[170:173], v[154:157], v[82:97]
	ds_read_b64_tr_b16 v[206:207], v249 offset:28672
	ds_read_b64_tr_b16 v[208:209], v249 offset:29184
	s_waitcnt lgkmcnt(10)
	v_mfma_f32_32x32x16_bf16 v[98:113], v[162:165], v[154:157], v[82:97]
	ds_read_b64_tr_b16 v[202:203], v249 offset:25600
	ds_read_b64_tr_b16 v[204:205], v249 offset:26112
	s_waitcnt lgkmcnt(11)
	v_mfma_f32_32x32x16_bf16 v[114:129], v[174:177], v[150:153], v[114:129]
	ds_read_b64_tr_b16 v[198:199], v249 offset:29696
	ds_read_b64_tr_b16 v[200:201], v249 offset:30208
	s_waitcnt lgkmcnt(12)
	v_mfma_f32_32x32x16_bf16 v[98:113], v[166:169], v[150:153], v[98:113]
	ds_read_b64_tr_b16 v[194:195], v249 offset:26624
	ds_read_b64_tr_b16 v[196:197], v249 offset:27136
	s_waitcnt lgkmcnt(13)
	v_mfma_f32_32x32x16_bf16 v[114:129], v[182:185], v[146:149], v[114:129]
	ds_read_b64_tr_b16 v[158:159], v249 offset:30720
	ds_read_b64_tr_b16 v[160:161], v249 offset:31232
	s_waitcnt lgkmcnt(14)
	v_mfma_f32_32x32x16_bf16 v[98:113], v[178:181], v[146:149], v[98:113]
	ds_read_b64_tr_b16 v[12:13], v249 offset:27648
	ds_read_b64_tr_b16 v[14:15], v249 offset:28160
	s_waitcnt lgkmcnt(14)
	v_mfma_f32_32x32x16_bf16 v[114:129], v[190:193], v[142:145], v[114:129]
	ds_read_b64_tr_b16 v[8:9], v249 offset:31744
	ds_read_b64_tr_b16 v[10:11], v249 offset:32256
	v_mfma_f32_32x32x16_bf16 v[98:113], v[186:189], v[142:145], v[98:113]
	s_add_i32 s38, s87, 4
	s_cmp_ge_i32 s38, s85
	s_cselect_b64 s[46:47], -1, 0
	s_and_b64 vcc, exec, s[46:47]
	s_cbranch_vccnz .LBB0_328
	s_mov_b64 s[38:39], 0x120000
	v_lshl_add_u64 v[16:17], v[16:17], 0, s[38:39]
	s_add_i32 s38, s88, s76
	s_mov_b32 m0, s38
	s_nop 0
	global_load_lds_dwordx4 v[16:17], off
	s_andn2_b64 vcc, exec, s[0:1]
	s_cbranch_vccz .LBB0_329

.LBB0_307:
	s_nop 0
	v_max_f32_e32 v17, v115, v114
	v_max3_f32 v222, v116, v117, v99
	v_max3_f32 v17, v17, v98, v100
	v_max3_f32 v17, v17, v101, v118
	v_max3_f32 v222, v222, v120, v121
	v_max3_f32 v17, v17, v119, v102
	v_max3_f32 v222, v222, v104, v105
	v_max3_f32 v17, v17, v103, v122
	v_max3_f32 v222, v222, v124, v125
	v_max3_f32 v17, v17, v123, v106
	v_max3_f32 v222, v222, v108, v109
	v_max3_f32 v17, v17, v107, v126
	v_max3_f32 v222, v222, v128, v129
	v_max3_f32 v17, v17, v127, v110
	v_max3_f32 v222, v222, v112, v113
	v_max3_f32 v17, v17, v111, v222
	v_mov_b32_e32 v222, v17
	s_nop 1
	v_permlane32_swap_b32_e32 v17, v222
	v_max_f32_e32 v17, v17, v222
	v_cmp_lt_f32_e32 vcc, s79, v17
	s_cmp_lg_u64 vcc, 0
	v_add_f32_e32 v16, v243, v248
	s_cselect_b64 s[50:51], -1, 0
	s_cbranch_vccnz .LBB0_335

.LBB0_316:
	s_waitcnt lgkmcnt(6)
	v_mfma_f32_32x32x16_bf16 v[34:49], v[130:133], v[194:197], v[34:49]
	v_add_f32_e32 v17, v100, v114
	v_add_f32_e32 v17, v101, v17
	v_add_f32_e32 v17, v102, v17
	v_add_f32_e32 v17, v103, v17
	v_cvt_pk_bf16_f32 v134, v122, v123
	v_cvt_pk_bf16_f32 v135, v124, v125
	s_waitcnt lgkmcnt(4)
	v_mfma_f32_32x32x16_bf16 v[18:33], v[130:133], v[158:161], v[18:33]
	v_add_f32_e32 v17, v104, v17
	v_add_f32_e32 v17, v105, v17
	v_add_f32_e32 v17, v106, v17
	v_add_f32_e32 v17, v107, v17
	v_cvt_pk_bf16_f32 v136, v126, v127
	v_cvt_pk_bf16_f32 v137, v128, v129
	s_waitcnt lgkmcnt(2)
	v_mfma_f32_32x32x16_bf16 v[34:49], v[4:7], v[12:15], v[34:49]
	v_add_f32_e32 v17, v108, v17
	v_add_f32_e32 v17, v109, v17
	v_add_f32_e32 v17, v110, v17
	v_add_f32_e32 v17, v111, v17
	v_cvt_pk_bf16_f32 v130, v98, v99
	v_cvt_pk_bf16_f32 v131, v100, v101
	s_waitcnt lgkmcnt(0)
	v_mfma_f32_32x32x16_bf16 v[18:33], v[4:7], v[8:11], v[18:33]
	v_add_f32_e32 v12, v112, v17
	v_add_f32_e32 v12, v113, v12
	v_cvt_pk_bf16_f32 v132, v102, v103
	v_cvt_pk_bf16_f32 v133, v104, v105
	v_cvt_pk_bf16_f32 v158, v106, v107
	v_cvt_pk_bf16_f32 v159, v108, v109
	v_cvt_pk_bf16_f32 v160, v110, v111
	v_cvt_pk_bf16_f32 v161, v112, v113
	s_mov_b64 s[0:1], -1
	s_and_b64 vcc, exec, s[46:47]
	s_cbranch_vccz .LBB0_330
	s_and_b64 vcc, exec, s[42:43]
	s_cbranch_vccz .LBB0_319
	s_waitcnt vmcnt(0) lgkmcnt(0)
	s_barrier
	s_mov_b64 s[0:1], 0

.LBB0_329:
	s_add_i32 s0, s86, 0x4000
	s_and_b32 s0, s0, 0xffff
	v_lshl_add_u64 v[16:17], v[224:225], 0, s[30:31]
	s_add_i32 s0, s0, s77
	s_mov_b32 m0, s0
	s_nop 0
	global_load_lds_dwordx4 v[16:17], off
	v_lshl_add_u64 v[16:17], v[222:223], 0, s[30:31]
	s_addk_i32 s0, 0x2000
	s_mov_b32 m0, s0
	s_nop 0
	global_load_lds_dwordx4 v[16:17], off
	s_add_i32 s75, s75, 5
	s_cmp_lt_i32 s75, 0
	s_cbranch_scc0 .LBB0_304
	s_branch .LBB0_305

.LBB0_339:
	v_add_u32_e32 v2, s33, v242
	ds_read_b64_tr_b16 v[194:195], v2 offset:24576
	ds_read_b64_tr_b16 v[196:197], v2 offset:25088
	s_waitcnt lgkmcnt(9)
	v_mfma_f32_32x32x16_bf16 v[82:97], v[170:173], v[154:157], v[100:115]
	ds_read_b64_tr_b16 v[170:171], v2 offset:28672
	ds_read_b64_tr_b16 v[172:173], v2 offset:29184
	s_waitcnt lgkmcnt(10)
	v_mfma_f32_32x32x16_bf16 v[100:115], v[162:165], v[154:157], v[100:115]
	ds_read_b64_tr_b16 v[124:125], v2 offset:25600
	ds_read_b64_tr_b16 v[126:127], v2 offset:26112
	s_waitcnt lgkmcnt(11)
	v_mfma_f32_32x32x16_bf16 v[82:97], v[174:177], v[150:153], v[82:97]
	ds_read_b64_tr_b16 v[120:121], v2 offset:29696
	ds_read_b64_tr_b16 v[122:123], v2 offset:30208
	s_waitcnt lgkmcnt(12)
	v_mfma_f32_32x32x16_bf16 v[100:115], v[166:169], v[150:153], v[100:115]
	ds_read_b64_tr_b16 v[116:117], v2 offset:26624
	ds_read_b64_tr_b16 v[118:119], v2 offset:27136
	s_waitcnt lgkmcnt(13)
	v_mfma_f32_32x32x16_bf16 v[82:97], v[182:185], v[146:149], v[82:97]
	ds_read_b64_tr_b16 v[12:13], v2 offset:30720
	ds_read_b64_tr_b16 v[14:15], v2 offset:31232
	s_waitcnt lgkmcnt(14)
	v_mfma_f32_32x32x16_bf16 v[100:115], v[178:181], v[146:149], v[100:115]
	ds_read_b64_tr_b16 v[8:9], v2 offset:27648
	ds_read_b64_tr_b16 v[10:11], v2 offset:28160
	s_waitcnt lgkmcnt(14)
	v_mfma_f32_32x32x16_bf16 v[82:97], v[190:193], v[142:145], v[82:97]
	ds_read_b64_tr_b16 v[4:5], v2 offset:31744
	ds_read_b64_tr_b16 v[6:7], v2 offset:32256
	v_mfma_f32_32x32x16_bf16 v[100:115], v[186:189], v[142:145], v[100:115]
	v_or_b32_e32 v17, 0xe0, v239
	v_or_b32_e32 v16, 0xc0, v239
	v_cmp_le_i32_e32 vcc, v17, v238
	s_nop 8
	v_cndmask_b32_e32 v99, v227, v100, vcc
	v_cmp_lt_i32_e32 vcc, v16, v238
	s_nop 1
	v_cndmask_b32_e32 v83, v227, v83, vcc
	v_cmp_le_i32_e32 vcc, v16, v238
	v_or_b32_e32 v16, 0xe1, v239
	s_nop 0
	v_cndmask_b32_e32 v82, v227, v82, vcc
	v_cmp_le_i32_e32 vcc, v16, v238
	v_or_b32_e32 v16, 0xc2, v239
	s_nop 0
	v_cndmask_b32_e32 v100, v227, v101, vcc
	v_cmp_le_i32_e32 vcc, v16, v238
	v_or_b32_e32 v16, 0xe2, v239
	s_nop 0
	v_cndmask_b32_e32 v101, v227, v84, vcc
	v_cmp_le_i32_e32 vcc, v16, v238
	v_or_b32_e32 v16, 0xc3, v239
	s_nop 0
	v_cndmask_b32_e32 v142, v227, v102, vcc
	v_cmp_le_i32_e32 vcc, v16, v238
	v_or_b32_e32 v16, 0xe3, v239
	s_nop 0
	v_cndmask_b32_e32 v143, v227, v85, vcc
	v_cmp_le_i32_e32 vcc, v16, v238
	v_or_b32_e32 v16, 0xc8, v239
	s_nop 0
	v_cndmask_b32_e32 v144, v227, v103, vcc
	v_cmp_le_i32_e32 vcc, v16, v238
	v_or_b32_e32 v16, 0xe8, v239
	s_nop 0
	v_cndmask_b32_e32 v102, v227, v86, vcc
	v_cmp_le_i32_e32 vcc, v16, v238
	v_or_b32_e32 v16, 0xc9, v239
	s_nop 0
	v_cndmask_b32_e32 v86, v227, v104, vcc
	v_cmp_le_i32_e32 vcc, v16, v238
	v_or_b32_e32 v16, 0xe9, v239
	s_nop 0
	v_cndmask_b32_e32 v103, v227, v87, vcc
	v_cmp_le_i32_e32 vcc, v16, v238
	v_or_b32_e32 v16, 0xca, v239
	s_nop 0
	v_cndmask_b32_e32 v87, v227, v105, vcc
	v_cmp_le_i32_e32 vcc, v16, v238
	v_or_b32_e32 v16, 0xea, v239
	s_nop 0
	v_cndmask_b32_e32 v104, v227, v88, vcc
	v_cmp_le_i32_e32 vcc, v16, v238
	v_or_b32_e32 v16, 0xcb, v239
	s_nop 0
	v_cndmask_b32_e32 v88, v227, v106, vcc
	v_cmp_le_i32_e32 vcc, v16, v238
	v_or_b32_e32 v16, 0xeb, v239
	s_nop 0
	v_cndmask_b32_e32 v105, v227, v89, vcc
	v_cmp_le_i32_e32 vcc, v16, v238
	v_or_b32_e32 v16, 0xd0, v239
	s_nop 0
	v_cndmask_b32_e32 v89, v227, v107, vcc
	v_cmp_le_i32_e32 vcc, v16, v238
	v_or_b32_e32 v16, 0xf0, v239
	s_nop 0
	v_cndmask_b32_e32 v106, v227, v90, vcc
	v_cmp_le_i32_e32 vcc, v16, v238
	v_or_b32_e32 v16, 0xd1, v239
	s_nop 0
	v_cndmask_b32_e32 v90, v227, v108, vcc
	v_cmp_le_i32_e32 vcc, v16, v238
	v_or_b32_e32 v16, 0xf1, v239
	s_nop 0
	v_cndmask_b32_e32 v107, v227, v91, vcc
	v_cmp_le_i32_e32 vcc, v16, v238
	v_or_b32_e32 v16, 0xd2, v239
	s_nop 0
	v_cndmask_b32_e32 v91, v227, v109, vcc
	v_cmp_le_i32_e32 vcc, v16, v238
	v_or_b32_e32 v16, 0xf2, v239
	s_nop 0
	v_cndmask_b32_e32 v108, v227, v92, vcc
	v_cmp_le_i32_e32 vcc, v16, v238
	v_or_b32_e32 v16, 0xd3, v239
	s_nop 0
	v_cndmask_b32_e32 v92, v227, v110, vcc
	v_cmp_le_i32_e32 vcc, v16, v238
	v_or_b32_e32 v16, 0xf3, v239
	s_nop 0
	v_cndmask_b32_e32 v109, v227, v93, vcc
	v_cmp_le_i32_e32 vcc, v16, v238
	v_or_b32_e32 v16, 0xd8, v239
	s_nop 0
	v_cndmask_b32_e32 v93, v227, v111, vcc
	v_cmp_le_i32_e32 vcc, v16, v238
	v_or_b32_e32 v16, 0xf8, v239
	s_nop 0
	v_cndmask_b32_e32 v110, v227, v94, vcc
	v_cmp_le_i32_e32 vcc, v16, v238
	v_or_b32_e32 v16, 0xd9, v239
	s_nop 0
	v_cndmask_b32_e32 v94, v227, v112, vcc
	v_cmp_le_i32_e32 vcc, v16, v238
	v_or_b32_e32 v16, 0xf9, v239
	s_nop 0
	v_cndmask_b32_e32 v111, v227, v95, vcc
	v_cmp_le_i32_e32 vcc, v16, v238
	v_or_b32_e32 v16, 0xda, v239
	s_nop 0
	v_cndmask_b32_e32 v95, v227, v113, vcc
	v_cmp_le_i32_e32 vcc, v16, v238
	v_or_b32_e32 v16, 0xfa, v239
	s_nop 0
	v_cndmask_b32_e32 v112, v227, v96, vcc
	v_cmp_le_i32_e32 vcc, v16, v238
	v_or_b32_e32 v16, 0xdb, v239
	s_nop 0
	v_cndmask_b32_e32 v96, v227, v114, vcc
	v_cmp_le_i32_e32 vcc, v16, v238
	v_sub_u32_e32 v16, v238, v239
	v_lshl_add_u32 v145, v16, 2, s40
	v_cndmask_b32_e32 v113, v227, v97, vcc
	v_or_b32_e32 v97, 0xfb, v239
	v_cmp_le_i32_e32 vcc, v97, v238
	ds_read2_b32 v[16:17], v145 offset0:63 offset1:64
	ds_read2_b32 v[84:85], v145 offset0:31 offset1:32
	v_cndmask_b32_e32 v97, v227, v115, vcc
	ds_read2_b32 v[114:115], v145 offset0:61 offset1:62
	ds_read2_b32 v[128:129], v145 offset0:29 offset1:30
	s_waitcnt lgkmcnt(3)
	v_add_f32_e32 v98, v82, v17
	s_waitcnt lgkmcnt(2)
	v_add_f32_e32 v82, v99, v85
	v_add_f32_e32 v99, v83, v16
	v_add_f32_e32 v83, v100, v84
	s_waitcnt lgkmcnt(1)
	v_add_f32_e32 v100, v101, v115
	s_waitcnt lgkmcnt(0)
	v_add_f32_e32 v84, v142, v129
	v_add_f32_e32 v101, v143, v114
	v_add_f32_e32 v85, v144, v128
	s_nop 0
	ds_read2_b32 v[16:17], v145 offset0:55 offset1:56
	ds_read2_b32 v[114:115], v145 offset0:23 offset1:24
	ds_read2_b32 v[128:129], v145 offset0:53 offset1:54
	ds_read2_b32 v[142:143], v145 offset0:21 offset1:22
	s_waitcnt lgkmcnt(3)
	v_add_f32_e32 v102, v102, v17
	s_waitcnt lgkmcnt(2)
	v_add_f32_e32 v86, v86, v115
	v_add_f32_e32 v103, v103, v16
	v_add_f32_e32 v87, v87, v114
	s_waitcnt lgkmcnt(1)
	v_add_f32_e32 v104, v104, v129
	s_waitcnt lgkmcnt(0)
	v_add_f32_e32 v88, v88, v143
	v_add_f32_e32 v105, v105, v128
	v_add_f32_e32 v89, v89, v142
	s_nop 0
	ds_read2_b32 v[16:17], v145 offset0:47 offset1:48
	ds_read2_b32 v[114:115], v145 offset0:15 offset1:16
	ds_read2_b32 v[128:129], v145 offset0:45 offset1:46
	ds_read2_b32 v[142:143], v145 offset0:13 offset1:14
	s_waitcnt lgkmcnt(3)
	v_add_f32_e32 v106, v106, v17
	s_waitcnt lgkmcnt(2)
	v_add_f32_e32 v90, v90, v115
	v_add_f32_e32 v107, v107, v16
	v_add_f32_e32 v91, v91, v114
	s_waitcnt lgkmcnt(1)
	v_add_f32_e32 v108, v108, v129
	s_waitcnt lgkmcnt(0)
	v_add_f32_e32 v92, v92, v143
	v_add_f32_e32 v109, v109, v128
	v_add_f32_e32 v93, v93, v142
	s_nop 0
	ds_read2_b32 v[16:17], v145 offset0:39 offset1:40
	ds_read2_b32 v[114:115], v145 offset0:7 offset1:8
	ds_read2_b32 v[128:129], v145 offset0:37 offset1:38
	ds_read2_b32 v[142:143], v145 offset0:5 offset1:6
	s_waitcnt lgkmcnt(3)
	v_add_f32_e32 v110, v110, v17
	s_waitcnt lgkmcnt(2)
	v_add_f32_e32 v94, v94, v115
	v_add_f32_e32 v111, v111, v16
	v_add_f32_e32 v95, v95, v114
	s_waitcnt lgkmcnt(1)
	v_add_f32_e32 v112, v112, v129
	s_waitcnt lgkmcnt(0)
	v_add_f32_e32 v96, v96, v143
	v_add_f32_e32 v113, v113, v128
	v_add_f32_e32 v97, v97, v142
	s_nop 0
	s_nop 0
	v_max_f32_e32 v16, v99, v98
	v_max3_f32 v17, v100, v101, v83
	v_max3_f32 v16, v16, v82, v84
	v_max3_f32 v16, v16, v85, v102
	v_max3_f32 v17, v17, v104, v105
	v_max3_f32 v16, v16, v103, v86
	v_max3_f32 v17, v17, v88, v89
	v_max3_f32 v16, v16, v87, v106
	v_max3_f32 v17, v17, v108, v109
	v_max3_f32 v16, v16, v107, v90
	v_max3_f32 v17, v17, v92, v93
	v_max3_f32 v16, v16, v91, v110
	v_max3_f32 v17, v17, v112, v113
	v_max3_f32 v16, v16, v111, v94
	v_max3_f32 v17, v17, v96, v97
	v_max3_f32 v16, v16, v95, v17
	v_mov_b32_e32 v17, v16
	s_nop 1
	v_permlane32_swap_b32_e32 v16, v17
	v_max_f32_e32 v16, v16, v17
	v_cmp_lt_f32_e32 vcc, s79, v16
	s_cmp_lg_u64 vcc, 0
	s_cselect_b64 s[0:1], -1, 0
	s_cbranch_vccnz .LBB0_346
.LBB0_340:
	v_mfma_f32_32x32x16_bf16 v[66:81], v[138:141], v[194:197], v[66:81]
	v_exp_f32_e32 v98, v98
	v_exp_f32_e32 v99, v99
	v_exp_f32_e32 v100, v100
	v_exp_f32_e32 v101, v101
	ds_read_b64_tr_b16 v[142:143], v2 offset:32768
	ds_read_b64_tr_b16 v[144:145], v2 offset:33280
	v_mfma_f32_32x32x16_bf16 v[50:65], v[138:141], v[170:173], v[50:65]
	v_exp_f32_e32 v102, v102
	v_exp_f32_e32 v103, v103
	v_exp_f32_e32 v104, v104
	v_exp_f32_e32 v105, v105
	ds_read_b64_tr_b16 v[146:147], v2 offset:36864
	ds_read_b64_tr_b16 v[148:149], v2 offset:37376
	v_mfma_f32_32x32x16_bf16 v[66:81], v[134:137], v[124:127], v[66:81]
	v_exp_f32_e32 v106, v106
	v_exp_f32_e32 v107, v107
	v_exp_f32_e32 v108, v108
	v_exp_f32_e32 v109, v109
	ds_read_b64_tr_b16 v[124:125], v2 offset:33792
	ds_read_b64_tr_b16 v[126:127], v2 offset:34304
	v_mfma_f32_32x32x16_bf16 v[50:65], v[134:137], v[120:123], v[50:65]
	v_exp_f32_e32 v110, v110
	v_exp_f32_e32 v111, v111
	v_exp_f32_e32 v112, v112
	v_exp_f32_e32 v113, v113
	ds_read_b64_tr_b16 v[120:121], v2 offset:37888
	ds_read_b64_tr_b16 v[122:123], v2 offset:38400
	v_mfma_f32_32x32x16_bf16 v[66:81], v[130:133], v[116:119], v[66:81]
	v_exp_f32_e32 v82, v82
	v_exp_f32_e32 v83, v83
	v_exp_f32_e32 v84, v84
	v_exp_f32_e32 v85, v85
	ds_read_b64_tr_b16 v[114:115], v2 offset:34816
	ds_read_b64_tr_b16 v[116:117], v2 offset:35328
	v_mfma_f32_32x32x16_bf16 v[50:65], v[130:133], v[12:15], v[50:65]
	v_exp_f32_e32 v86, v86
	v_exp_f32_e32 v87, v87
	v_exp_f32_e32 v88, v88
	v_exp_f32_e32 v89, v89
	ds_read_b64_tr_b16 v[12:13], v2 offset:38912
	ds_read_b64_tr_b16 v[14:15], v2 offset:39424
	v_mfma_f32_32x32x16_bf16 v[66:81], v[158:161], v[8:11], v[66:81]
	v_exp_f32_e32 v90, v90
	v_exp_f32_e32 v91, v91
	v_exp_f32_e32 v92, v92
	v_exp_f32_e32 v93, v93
	ds_read_b64_tr_b16 v[8:9], v2 offset:35840
	ds_read_b64_tr_b16 v[10:11], v2 offset:36352
	v_mfma_f32_32x32x16_bf16 v[50:65], v[158:161], v[4:7], v[50:65]
	v_exp_f32_e32 v94, v94
	v_exp_f32_e32 v95, v95
	v_exp_f32_e32 v96, v96
	v_exp_f32_e32 v97, v97
	ds_read_b64_tr_b16 v[4:5], v2 offset:39936
	ds_read_b64_tr_b16 v[6:7], v2 offset:40448
	v_add_f32_e32 v2, v98, v99
	s_waitcnt lgkmcnt(14)
	v_mfma_f32_32x32x16_bf16 v[34:49], v[138:141], v[142:145], v[34:49]
	v_add_f32_e32 v2, v100, v2
	v_add_f32_e32 v2, v101, v2
	v_add_f32_e32 v2, v102, v2
	v_add_f32_e32 v2, v103, v2
	s_waitcnt lgkmcnt(12)
	v_mfma_f32_32x32x16_bf16 v[18:33], v[138:141], v[146:149], v[18:33]
	v_add_f32_e32 v2, v104, v2
	v_add_f32_e32 v2, v105, v2
	v_add_f32_e32 v2, v106, v2
	v_add_f32_e32 v2, v107, v2
	s_waitcnt lgkmcnt(10)
	v_mfma_f32_32x32x16_bf16 v[34:49], v[134:137], v[124:127], v[34:49]
	v_add_f32_e32 v2, v108, v2
	v_add_f32_e32 v2, v109, v2
	v_add_f32_e32 v2, v110, v2
	v_add_f32_e32 v2, v111, v2
	v_cvt_pk_bf16_f32 v138, v98, v99
	v_cvt_pk_bf16_f32 v139, v100, v101
	s_waitcnt lgkmcnt(8)
	v_mfma_f32_32x32x16_bf16 v[18:33], v[134:137], v[120:123], v[18:33]
	v_add_f32_e32 v2, v112, v2
	v_add_f32_e32 v2, v113, v2
	v_add_f32_e32 v2, v82, v2
	v_add_f32_e32 v2, v83, v2
	v_cvt_pk_bf16_f32 v140, v102, v103
	v_cvt_pk_bf16_f32 v141, v104, v105
	s_waitcnt lgkmcnt(6)
	v_mfma_f32_32x32x16_bf16 v[34:49], v[130:133], v[114:117], v[34:49]
	v_add_f32_e32 v2, v84, v2
	v_add_f32_e32 v2, v85, v2
	v_add_f32_e32 v2, v86, v2
	v_add_f32_e32 v2, v87, v2
	v_cvt_pk_bf16_f32 v134, v106, v107
	v_cvt_pk_bf16_f32 v135, v108, v109
	s_waitcnt lgkmcnt(4)
	v_mfma_f32_32x32x16_bf16 v[18:33], v[130:133], v[12:15], v[18:33]
	v_add_f32_e32 v2, v88, v2
	v_add_f32_e32 v2, v89, v2
	v_add_f32_e32 v2, v90, v2
	v_add_f32_e32 v2, v91, v2
	v_cvt_pk_bf16_f32 v136, v110, v111
	v_cvt_pk_bf16_f32 v137, v112, v113
	s_waitcnt lgkmcnt(2)
	v_mfma_f32_32x32x16_bf16 v[34:49], v[158:161], v[8:11], v[34:49]
	v_add_f32_e32 v2, v92, v2
	v_add_f32_e32 v2, v93, v2
	v_add_f32_e32 v2, v94, v2
	v_add_f32_e32 v2, v95, v2
	v_cvt_pk_bf16_f32 v130, v82, v83
	v_cvt_pk_bf16_f32 v131, v84, v85
	s_waitcnt lgkmcnt(0)
	v_mfma_f32_32x32x16_bf16 v[18:33], v[158:161], v[4:7], v[18:33]
	v_add_f32_e32 v2, v96, v2
	v_add_f32_e32 v2, v97, v2
	v_cvt_pk_bf16_f32 v132, v86, v87
	v_cvt_pk_bf16_f32 v133, v88, v89
	v_cvt_pk_bf16_f32 v4, v90, v91
	v_cvt_pk_bf16_f32 v5, v92, v93
	v_cvt_pk_bf16_f32 v6, v94, v95
	v_cvt_pk_bf16_f32 v7, v96, v97
	s_andn2_b64 vcc, exec, s[0:1]
	s_cbranch_vccnz .LBB0_342
	s_waitcnt lgkmcnt(0)
	ds_read2_b32 v[8:9], v234 offset1:1
	ds_read2_b32 v[10:11], v234 offset0:2 offset1:3
	ds_read2_b32 v[12:13], v234 offset0:8 offset1:9
	ds_read2_b32 v[14:15], v234 offset0:10 offset1:11
	s_waitcnt lgkmcnt(3)
	v_mul_f32_e32 v66, v66, v8
	v_mul_f32_e32 v50, v50, v8
	v_mul_f32_e32 v34, v34, v8
	v_mul_f32_e32 v18, v18, v8
	v_mul_f32_e32 v67, v67, v9
	v_mul_f32_e32 v51, v51, v9
	v_mul_f32_e32 v35, v35, v9
	v_mul_f32_e32 v19, v19, v9
	s_waitcnt lgkmcnt(2)
	v_mul_f32_e32 v68, v68, v10
	v_mul_f32_e32 v52, v52, v10
	v_mul_f32_e32 v36, v36, v10
	v_mul_f32_e32 v20, v20, v10
	v_mul_f32_e32 v69, v69, v11
	v_mul_f32_e32 v53, v53, v11
	v_mul_f32_e32 v37, v37, v11
	v_mul_f32_e32 v21, v21, v11
	s_waitcnt lgkmcnt(1)
	v_mul_f32_e32 v70, v70, v12
	v_mul_f32_e32 v54, v54, v12
	v_mul_f32_e32 v38, v38, v12
	v_mul_f32_e32 v22, v22, v12
	v_mul_f32_e32 v71, v71, v13
	v_mul_f32_e32 v55, v55, v13
	v_mul_f32_e32 v39, v39, v13
	v_mul_f32_e32 v23, v23, v13
	s_waitcnt lgkmcnt(0)
	v_mul_f32_e32 v72, v72, v14
	v_mul_f32_e32 v56, v56, v14
	v_mul_f32_e32 v40, v40, v14
	v_mul_f32_e32 v24, v24, v14
	v_mul_f32_e32 v73, v73, v15
	v_mul_f32_e32 v57, v57, v15
	v_mul_f32_e32 v41, v41, v15
	ds_read2_b32 v[8:9], v234 offset0:16 offset1:17
	v_mul_f32_e32 v25, v25, v15
	ds_read2_b32 v[10:11], v234 offset0:18 offset1:19
	ds_read2_b32 v[12:13], v234 offset0:24 offset1:25
	ds_read2_b32 v[14:15], v234 offset0:26 offset1:27
	s_waitcnt lgkmcnt(3)
	v_mul_f32_e32 v74, v74, v8
	v_mul_f32_e32 v58, v58, v8
	v_mul_f32_e32 v42, v42, v8
	v_mul_f32_e32 v26, v26, v8
	v_mul_f32_e32 v75, v75, v9
	v_mul_f32_e32 v59, v59, v9
	v_mul_f32_e32 v43, v43, v9
	v_mul_f32_e32 v27, v27, v9
	s_waitcnt lgkmcnt(2)
	v_mul_f32_e32 v76, v76, v10
	v_mul_f32_e32 v60, v60, v10
	v_mul_f32_e32 v44, v44, v10
	v_mul_f32_e32 v28, v28, v10
	v_mul_f32_e32 v77, v77, v11
	v_mul_f32_e32 v61, v61, v11
	v_mul_f32_e32 v45, v45, v11
	v_mul_f32_e32 v29, v29, v11
	s_waitcnt lgkmcnt(1)
	v_mul_f32_e32 v78, v78, v12
	v_mul_f32_e32 v62, v62, v12
	v_mul_f32_e32 v46, v46, v12
	v_mul_f32_e32 v30, v30, v12
	v_mul_f32_e32 v79, v79, v13
	v_mul_f32_e32 v63, v63, v13
	v_mul_f32_e32 v47, v47, v13
	v_mul_f32_e32 v31, v31, v13
	s_waitcnt lgkmcnt(0)
	v_mul_f32_e32 v80, v80, v14
	v_mul_f32_e32 v64, v64, v14
	v_mul_f32_e32 v48, v48, v14
	v_mul_f32_e32 v32, v32, v14
	v_mul_f32_e32 v81, v81, v15
	v_mul_f32_e32 v65, v65, v15
	v_mul_f32_e32 v49, v49, v15
	v_mul_f32_e32 v33, v33, v15

.LBB0_873:
	s_lshr_b32 s42, s21, 1
	s_bitcmp0_b32 s21, 0
	s_cselect_b32 s63, s50, s47
	s_lshl_b32 s0, s42, 7
	s_add_u32 s3, s51, s0
	s_addc_u32 s29, s52, 0
	s_add_u32 s31, s53, s0
	v_mov_b32_e32 v36, v0
	s_mov_b32 s30, s63
	s_mov_b32 s0, s4
	s_addc_u32 s35, s55, 0
	s_ashr_i32 s1, s0, 31
	v_readfirstlane_b32 s2, v36
	s_lshl_b64 s[26:27], s[0:1], 14
	s_lshl_b32 s1, s30, 8
	s_ashr_i32 s33, s2, 6
	s_ashr_i32 s28, s1, 31
	s_add_u32 s26, s26, s1
	s_addc_u32 s27, s27, s28
	s_lshl_b32 s38, s33, 5
	s_ashr_i32 s28, s38, 31
	s_add_u32 s26, s26, s38
	s_addc_u32 s27, s27, s28
	s_mul_i32 s28, s27, 0x1200
	s_mul_hi_u32 s34, s26, 0x1200
	s_add_i32 s34, s34, s28
	s_mul_i32 s28, s26, 0x1200
	s_add_u32 s28, s3, s28
	s_addc_u32 s29, s29, s34
	s_mul_hi_i32 s3, s0, 0x4800000
	s_mul_i32 s0, s0, 0x4800000
	v_and_b32_e32 v230, 63, v36
	s_add_u32 s34, s31, s0
	s_addc_u32 s35, s35, s3
	v_mul_u32_u24_e32 v2, 0x900, v230
	s_add_u32 s36, s56, s0
	v_lshlrev_b32_e32 v2, 1, v2
	s_addc_u32 s37, s57, s3
	v_lshl_add_u64 v[4:5], s[34:35], 0, v[2:3]
	s_lshl_b32 s34, s33, 3
	s_lshl_b32 s0, s33, 4
	v_bfe_u32 v2, v36, 2, 4
	s_ashr_i32 s35, s34, 31
	v_and_or_b32 v2, s0, 48, v2
	s_ashr_i32 s0, s2, 3
	v_lshl_add_u64 v[216:217], s[34:35], 1, v[4:5]
	s_and_b32 s34, s0, 0xffffffe0
	v_mul_u32_u24_e32 v2, 0x900, v2
	s_ashr_i32 s35, s34, 31
	s_lshl_b32 s0, s33, 10
	v_lshlrev_b32_e32 v2, 1, v2
	v_lshlrev_b32_e32 v232, 3, v36
	s_cmp_lg_u32 0, -1
	v_lshl_add_u64 v[4:5], s[36:37], 0, v[2:3]
	v_and_b32_e32 v233, 24, v232
	s_cselect_b32 s3, 0, 0
	v_and_b32_e32 v231, 31, v36
	v_lshl_add_u64 v[4:5], s[34:35], 1, v[4:5]
	v_lshlrev_b32_e32 v2, 1, v233
	s_add_i32 s76, s0, s3
	s_mov_b32 m0, s76
	s_nop 0
	global_load_lds_dwordx4 v[216:217], off
	v_lshl_add_u64 v[218:219], v[4:5], 0, v[2:3]
	s_add_i32 s77, s76, 0x6000
	s_mov_b32 m0, s77
	s_nop 0
	global_load_lds_dwordx4 v[218:219], off
	s_mov_b64 s[34:35], 0x80
	v_mul_u32_u24_e32 v2, 0x900, v231
	v_bfe_u32 v229, v36, 5, 1
	v_lshl_add_u64 v[220:221], v[218:219], 0, s[34:35]
	s_add_i32 s3, s76, 0x8000
	s_mov_b32 m0, s3
	s_nop 0
	global_load_lds_dwordx4 v[220:221], off
	v_lshlrev_b32_e32 v2, 1, v2
	v_lshl_add_u64 v[4:5], v[216:217], 0, s[18:19]
	s_add_i32 s3, s76, 0x2000
	s_mov_b32 m0, s3
	s_nop 0
	global_load_lds_dwordx4 v[4:5], off
	v_lshl_or_b32 v2, v229, 4, v2
	global_load_dwordx4 v[154:157], v2, s[28:29]
	global_load_dwordx4 v[150:153], v2, s[28:29] offset:32
	global_load_dwordx4 v[146:149], v2, s[28:29] offset:64
	global_load_dwordx4 v[142:145], v2, s[28:29] offset:96
	s_mov_b64 s[28:29], 0x48080
	v_lshlrev_b32_e32 v2, 10, v229
	v_lshlrev_b32_e32 v4, 4, v231
	v_add3_u32 v240, 0, v2, v4
	v_lshl_add_u64 v[4:5], v[216:217], 0, s[22:23]
	s_add_i32 s3, s76, 0x4000
	v_lshl_add_u64 v[8:9], v[218:219], 0, s[28:29]
	s_mov_b32 m0, s3
	s_nop 0
	global_load_lds_dwordx4 v[4:5], off
	s_add_i32 s31, s76, 0xa000
	v_lshl_add_u64 v[6:7], v[218:219], 0, s[18:19]
	s_mov_b32 m0, s31
	s_nop 0
	global_load_lds_dwordx4 v[6:7], off
	s_add_i32 s34, s76, 0xc000
	s_mov_b32 m0, s34
	s_nop 0
	global_load_lds_dwordx4 v[8:9], off
	s_waitcnt vmcnt(6) lgkmcnt(0)
	s_barrier
	ds_read_b128 v[4:7], v240
	ds_read_b128 v[8:11], v240 offset:512
	ds_read_b128 v[38:41], v240 offset:2048
	ds_read_b128 v[42:45], v240 offset:2560
	s_add_i32 s3, s1, 0x100
	s_ashr_i32 s79, s3, 6
	v_lshlrev_b32_e32 v239, 2, v229
	v_or_b32_e32 v238, s38, v231
	s_cmp_gt_i32 s79, 4
	s_waitcnt vmcnt(3) lgkmcnt(3)
	v_mfma_f32_32x32x16_bf16 v[20:35], v[4:7], v[154:157], 0
	s_waitcnt lgkmcnt(2)
	v_mfma_f32_32x32x16_bf16 v[4:19], v[8:11], v[154:157], 0
	s_waitcnt vmcnt(2) lgkmcnt(1)
	v_mfma_f32_32x32x16_bf16 v[20:35], v[38:41], v[150:153], v[20:35]
	s_waitcnt lgkmcnt(0)
	v_mfma_f32_32x32x16_bf16 v[4:19], v[42:45], v[150:153], v[4:19]
	ds_read_b128 v[38:41], v240 offset:4096
	ds_read_b128 v[42:45], v240 offset:4608
	s_waitcnt vmcnt(1) lgkmcnt(1)
	v_mfma_f32_32x32x16_bf16 v[20:35], v[38:41], v[146:149], v[20:35]
	s_waitcnt lgkmcnt(0)
	v_mfma_f32_32x32x16_bf16 v[4:19], v[42:45], v[146:149], v[4:19]
	ds_read_b128 v[38:41], v240 offset:6144
	ds_read_b128 v[42:45], v240 offset:6656
	s_waitcnt vmcnt(0) lgkmcnt(1)
	v_mfma_f32_32x32x16_bf16 v[20:35], v[38:41], v[142:145], v[20:35]
	s_waitcnt lgkmcnt(0)
	v_mfma_f32_32x32x16_bf16 v[4:19], v[42:45], v[142:145], v[4:19]
	s_nop 15
	s_nop 7
	s_cbranch_scc1 .LBB0_875
	v_subrev_u32_e32 v2, s1, v239
	v_or_b32_e32 v37, 32, v2
	v_cmp_le_i32_e32 vcc, v37, v238
	v_or_b32_e32 v37, 33, v2
	s_nop 6
	v_cndmask_b32_e32 v4, v227, v4, vcc
	v_cmp_lt_i32_e32 vcc, v2, v238
	s_nop 1
	v_cndmask_b32_e32 v21, v227, v21, vcc
	v_cmp_le_i32_e32 vcc, v2, v238
	s_nop 1
	v_cndmask_b32_e32 v20, v227, v20, vcc
	v_cmp_le_i32_e32 vcc, v37, v238
	v_or_b32_e32 v37, 2, v2
	s_nop 0
	v_cndmask_b32_e32 v5, v227, v5, vcc
	v_cmp_le_i32_e32 vcc, v37, v238
	v_or_b32_e32 v37, 34, v2
	s_nop 0
	v_cndmask_b32_e32 v22, v227, v22, vcc
	v_cmp_le_i32_e32 vcc, v37, v238
	v_or_b32_e32 v37, 3, v2
	s_nop 0
	v_cndmask_b32_e32 v6, v227, v6, vcc
	v_cmp_le_i32_e32 vcc, v37, v238
	v_or_b32_e32 v37, 35, v2
	s_nop 0
	v_cndmask_b32_e32 v23, v227, v23, vcc
	v_cmp_le_i32_e32 vcc, v37, v238
	v_or_b32_e32 v37, 8, v2
	s_nop 0
	v_cndmask_b32_e32 v7, v227, v7, vcc
	v_cmp_le_i32_e32 vcc, v37, v238
	v_or_b32_e32 v37, 40, v2
	s_nop 0
	v_cndmask_b32_e32 v24, v227, v24, vcc
	v_cmp_le_i32_e32 vcc, v37, v238
	v_or_b32_e32 v37, 9, v2
	s_nop 0
	v_cndmask_b32_e32 v8, v227, v8, vcc
	v_cmp_le_i32_e32 vcc, v37, v238
	v_or_b32_e32 v37, 41, v2
	s_nop 0
	v_cndmask_b32_e32 v25, v227, v25, vcc
	v_cmp_le_i32_e32 vcc, v37, v238
	v_or_b32_e32 v37, 10, v2
	s_nop 0
	v_cndmask_b32_e32 v9, v227, v9, vcc
	v_cmp_le_i32_e32 vcc, v37, v238
	v_or_b32_e32 v37, 42, v2
	s_nop 0
	v_cndmask_b32_e32 v26, v227, v26, vcc
	v_cmp_le_i32_e32 vcc, v37, v238
	v_or_b32_e32 v37, 11, v2
	s_nop 0
	v_cndmask_b32_e32 v10, v227, v10, vcc
	v_cmp_le_i32_e32 vcc, v37, v238
	v_or_b32_e32 v37, 43, v2
	s_nop 0
	v_cndmask_b32_e32 v27, v227, v27, vcc
	v_cmp_le_i32_e32 vcc, v37, v238
	v_or_b32_e32 v37, 16, v2
	s_nop 0
	v_cndmask_b32_e32 v11, v227, v11, vcc
	v_cmp_le_i32_e32 vcc, v37, v238
	v_or_b32_e32 v37, 48, v2
	s_nop 0
	v_cndmask_b32_e32 v28, v227, v28, vcc
	v_cmp_le_i32_e32 vcc, v37, v238
	v_or_b32_e32 v37, 17, v2
	s_nop 0
	v_cndmask_b32_e32 v12, v227, v12, vcc
	v_cmp_le_i32_e32 vcc, v37, v238
	v_or_b32_e32 v37, 49, v2
	s_nop 0
	v_cndmask_b32_e32 v29, v227, v29, vcc
	v_cmp_le_i32_e32 vcc, v37, v238
	v_or_b32_e32 v37, 18, v2
	s_nop 0
	v_cndmask_b32_e32 v13, v227, v13, vcc
	v_cmp_le_i32_e32 vcc, v37, v238
	v_or_b32_e32 v37, 50, v2
	s_nop 0
	v_cndmask_b32_e32 v30, v227, v30, vcc
	v_cmp_le_i32_e32 vcc, v37, v238
	v_or_b32_e32 v37, 19, v2
	s_nop 0
	v_cndmask_b32_e32 v14, v227, v14, vcc
	v_cmp_le_i32_e32 vcc, v37, v238
	v_or_b32_e32 v37, 51, v2
	s_nop 0
	v_cndmask_b32_e32 v31, v227, v31, vcc
	v_cmp_le_i32_e32 vcc, v37, v238
	v_or_b32_e32 v37, 24, v2
	s_nop 0
	v_cndmask_b32_e32 v15, v227, v15, vcc
	v_cmp_le_i32_e32 vcc, v37, v238
	v_or_b32_e32 v37, 56, v2
	s_nop 0
	v_cndmask_b32_e32 v32, v227, v32, vcc
	v_cmp_le_i32_e32 vcc, v37, v238
	v_or_b32_e32 v37, 25, v2
	s_nop 0
	v_cndmask_b32_e32 v16, v227, v16, vcc
	v_cmp_le_i32_e32 vcc, v37, v238
	v_or_b32_e32 v37, 57, v2
	s_nop 0
	v_cndmask_b32_e32 v33, v227, v33, vcc
	v_cmp_le_i32_e32 vcc, v37, v238
	v_or_b32_e32 v37, 26, v2
	s_nop 0
	v_cndmask_b32_e32 v17, v227, v17, vcc
	v_cmp_le_i32_e32 vcc, v37, v238
	v_or_b32_e32 v37, 58, v2
	s_nop 0
	v_cndmask_b32_e32 v34, v227, v34, vcc
	v_cmp_le_i32_e32 vcc, v37, v238
	v_or_b32_e32 v37, 27, v2
	v_or_b32_e32 v2, 59, v2
	v_cndmask_b32_e32 v18, v227, v18, vcc
	v_cmp_le_i32_e32 vcc, v37, v238
	s_nop 1
	v_cndmask_b32_e32 v35, v227, v35, vcc
	v_cmp_le_i32_e32 vcc, v2, v238
	s_nop 1
	v_cndmask_b32_e32 v19, v227, v19, vcc

.LBB0_877:
	s_waitcnt vmcnt(0) lgkmcnt(0)
	s_barrier
	v_lshl_add_u64 v[38:39], v[216:217], 0, s[24:25]
	s_mov_b32 m0, s76
	s_nop 0
	global_load_lds_dwordx4 v[38:39], off
	s_cmp_lg_u32 0, -1
	v_max3_f32 v2, v20, v21, v4
	s_cselect_b32 s1, 0, 0
	v_max3_f32 v37, v22, v23, v5
	v_max3_f32 v2, v2, v6, v7
	s_add_i32 s3, s1, s0
	v_max3_f32 v2, v2, v24, v25
	v_max3_f32 v37, v37, v26, v27
	v_lshl_add_u64 v[38:39], v[218:219], 0, s[22:23]
	s_add_i32 s0, s3, 0xe000
	s_mov_b32 m0, s0
	s_nop 0
	global_load_lds_dwordx4 v[38:39], off
	v_max3_f32 v2, v2, v8, v9
	v_max3_f32 v37, v37, v10, v11
	s_mov_b64 s[0:1], 0x90080
	v_max3_f32 v2, v2, v28, v29
	v_max3_f32 v37, v37, v30, v31
	v_lshl_add_u64 v[38:39], v[218:219], 0, s[0:1]
	s_add_i32 s3, s3, 0x10000
	s_mov_b32 m0, s3
	s_nop 0
	global_load_lds_dwordx4 v[38:39], off
	v_max3_f32 v2, v2, v12, v13
	v_max3_f32 v37, v37, v14, v15
	ds_read_b128 v[170:173], v240 offset:8192
	ds_read_b128 v[162:165], v240 offset:8704
	ds_read_b128 v[174:177], v240 offset:10240
	ds_read_b128 v[166:169], v240 offset:10752
	ds_read_b128 v[182:185], v240 offset:12288
	ds_read_b128 v[178:181], v240 offset:12800
	ds_read_b128 v[190:193], v240 offset:14336
	ds_read_b128 v[186:189], v240 offset:14848
	v_max3_f32 v2, v2, v32, v33
	v_max3_f32 v37, v37, v34, v35
	s_waitcnt vmcnt(3) lgkmcnt(0)
	s_barrier
	s_cmp_gt_i32 s79, 8
	v_max3_f32 v2, v2, v16, v17
	v_max3_f32 v37, v37, v18, v19
	s_mov_b64 s[0:1], -1
	v_max_f32_e32 v2, v2, v37
	s_nop 0
	v_mov_b32_e32 v37, v2
	s_nop 1
	v_permlane32_swap_b32_e32 v2, v37
	v_max_f32_e32 v2, v2, v37
	s_nop 0
	v_sub_f32_e32 v20, v20, v2
	v_sub_f32_e32 v37, v4, v2
	v_sub_f32_e32 v4, v21, v2
	v_sub_f32_e32 v21, v5, v2
	v_sub_f32_e32 v5, v22, v2
	v_sub_f32_e32 v22, v6, v2
	v_sub_f32_e32 v6, v23, v2
	v_sub_f32_e32 v23, v7, v2
	v_sub_f32_e32 v7, v24, v2
	v_sub_f32_e32 v24, v8, v2
	v_sub_f32_e32 v8, v25, v2
	v_sub_f32_e32 v25, v9, v2
	v_sub_f32_e32 v9, v26, v2
	v_sub_f32_e32 v26, v10, v2
	v_sub_f32_e32 v10, v27, v2
	v_sub_f32_e32 v27, v11, v2
	v_sub_f32_e32 v11, v28, v2
	v_sub_f32_e32 v28, v12, v2
	v_sub_f32_e32 v12, v29, v2
	v_sub_f32_e32 v29, v13, v2
	v_sub_f32_e32 v13, v30, v2
	v_sub_f32_e32 v30, v14, v2
	v_sub_f32_e32 v14, v31, v2
	v_sub_f32_e32 v31, v15, v2
	v_sub_f32_e32 v15, v32, v2
	v_sub_f32_e32 v32, v16, v2
	v_sub_f32_e32 v16, v33, v2
	v_sub_f32_e32 v33, v17, v2
	v_sub_f32_e32 v17, v34, v2
	v_sub_f32_e32 v34, v18, v2
	v_sub_f32_e32 v18, v35, v2
	v_add_f32_e32 v241, v3, v2
	v_sub_f32_e32 v35, v19, v2
	s_nop 0
	v_exp_f32_e32 v2, v20
	v_exp_f32_e32 v4, v4
	v_exp_f32_e32 v5, v5
	v_exp_f32_e32 v6, v6
	v_exp_f32_e32 v7, v7
	v_exp_f32_e32 v8, v8
	v_exp_f32_e32 v9, v9
	v_exp_f32_e32 v10, v10
	v_exp_f32_e32 v11, v11
	v_exp_f32_e32 v12, v12
	v_exp_f32_e32 v13, v13
	v_exp_f32_e32 v14, v14
	v_exp_f32_e32 v15, v15
	v_exp_f32_e32 v16, v16
	v_exp_f32_e32 v17, v17
	v_exp_f32_e32 v18, v18
	v_exp_f32_e32 v19, v37
	v_exp_f32_e32 v20, v21
	v_exp_f32_e32 v21, v22
	v_exp_f32_e32 v22, v23
	v_exp_f32_e32 v23, v24
	v_exp_f32_e32 v24, v25
	v_exp_f32_e32 v25, v26
	v_exp_f32_e32 v26, v27
	v_exp_f32_e32 v27, v28
	v_exp_f32_e32 v28, v29
	v_exp_f32_e32 v29, v30
	v_exp_f32_e32 v30, v31
	v_exp_f32_e32 v31, v32
	v_exp_f32_e32 v32, v33
	v_exp_f32_e32 v33, v34
	v_exp_f32_e32 v34, v35
	v_xor_b32_e32 v97, 0x80000000, v241
	v_cvt_pk_bf16_f32 v138, v2, v4
	v_cvt_pk_bf16_f32 v139, v5, v6
	v_cvt_pk_bf16_f32 v140, v7, v8
	v_cvt_pk_bf16_f32 v141, v9, v10
	v_cvt_pk_bf16_f32 v134, v11, v12
	v_cvt_pk_bf16_f32 v135, v13, v14
	v_cvt_pk_bf16_f32 v136, v15, v16
	v_cvt_pk_bf16_f32 v137, v17, v18
	v_cvt_pk_bf16_f32 v130, v19, v20
	v_cvt_pk_bf16_f32 v131, v21, v22
	v_cvt_pk_bf16_f32 v132, v23, v24
	v_cvt_pk_bf16_f32 v133, v25, v26
	v_cvt_pk_bf16_f32 v158, v27, v28
	v_cvt_pk_bf16_f32 v159, v29, v30
	v_cvt_pk_bf16_f32 v160, v31, v32
	v_cvt_pk_bf16_f32 v161, v33, v34
	s_cbranch_scc1 .LBB0_879
	v_mov_b32_e32 v96, v97
	v_mov_b32_e32 v82, v97
	v_mov_b32_e32 v83, v97
	v_mov_b32_e32 v84, v97
	v_mov_b32_e32 v85, v97
	v_mov_b32_e32 v86, v97
	v_mov_b32_e32 v87, v97
	v_mov_b32_e32 v88, v97
	v_mov_b32_e32 v89, v97
	v_mov_b32_e32 v90, v97
	v_mov_b32_e32 v91, v97
	v_mov_b32_e32 v92, v97
	v_mov_b32_e32 v93, v97
	v_mov_b32_e32 v94, v97
	v_mov_b32_e32 v95, v97
	v_mov_b64_e32 v[114:115], v[96:97]
	s_mov_b64 s[0:1], 0
	v_mov_b64_e32 v[112:113], v[94:95]
	v_mov_b64_e32 v[110:111], v[92:93]
	v_mov_b64_e32 v[108:109], v[90:91]
	v_mov_b64_e32 v[106:107], v[88:89]
	v_mov_b64_e32 v[104:105], v[86:87]
	v_mov_b64_e32 v[102:103], v[84:85]
	v_mov_b64_e32 v[100:101], v[82:83]

.LBB0_882:
	v_add_u32_e32 v2, s43, v242
	ds_read_b64_tr_b16 v[202:203], v2 offset:24576
	ds_read_b64_tr_b16 v[204:205], v2 offset:25088
	s_waitcnt lgkmcnt(9)
	v_mfma_f32_32x32x16_bf16 v[114:129], v[170:173], v[154:157], v[82:97]
	ds_read_b64_tr_b16 v[198:199], v2 offset:28672
	ds_read_b64_tr_b16 v[200:201], v2 offset:29184
	s_waitcnt lgkmcnt(10)
	v_mfma_f32_32x32x16_bf16 v[98:113], v[162:165], v[154:157], v[82:97]
	ds_read_b64_tr_b16 v[194:195], v2 offset:25600
	ds_read_b64_tr_b16 v[196:197], v2 offset:26112
	s_waitcnt lgkmcnt(11)
	v_mfma_f32_32x32x16_bf16 v[114:129], v[174:177], v[150:153], v[114:129]
	ds_read_b64_tr_b16 v[170:171], v2 offset:29696
	ds_read_b64_tr_b16 v[172:173], v2 offset:30208
	s_waitcnt lgkmcnt(12)
	v_mfma_f32_32x32x16_bf16 v[98:113], v[166:169], v[150:153], v[98:113]
	ds_read_b64_tr_b16 v[162:163], v2 offset:26624
	ds_read_b64_tr_b16 v[164:165], v2 offset:27136
	s_waitcnt lgkmcnt(13)
	v_mfma_f32_32x32x16_bf16 v[114:129], v[182:185], v[146:149], v[114:129]
	ds_read_b64_tr_b16 v[12:13], v2 offset:30720
	ds_read_b64_tr_b16 v[14:15], v2 offset:31232
	s_waitcnt lgkmcnt(14)
	v_mfma_f32_32x32x16_bf16 v[98:113], v[178:181], v[146:149], v[98:113]
	ds_read_b64_tr_b16 v[8:9], v2 offset:27648
	ds_read_b64_tr_b16 v[10:11], v2 offset:28160
	s_waitcnt lgkmcnt(14)
	v_mfma_f32_32x32x16_bf16 v[114:129], v[190:193], v[142:145], v[114:129]
	ds_read_b64_tr_b16 v[4:5], v2 offset:31744
	ds_read_b64_tr_b16 v[6:7], v2 offset:32256
	v_mfma_f32_32x32x16_bf16 v[98:113], v[186:189], v[142:145], v[98:113]
	s_mov_b32 s0, 0xfffb8000
	s_mov_b32 s1, -1
	v_lshl_add_u64 v[16:17], v[206:207], 0, s[0:1]
	s_add_i32 s0, s38, s76
	s_mov_b32 m0, s0
	s_nop 0
	global_load_lds_dwordx4 v[16:17], off
	s_nop 4
	v_max_f32_e32 v16, v115, v114
	v_max3_f32 v17, v116, v117, v99
	v_max3_f32 v16, v16, v98, v100
	v_max3_f32 v16, v16, v101, v118
	v_max3_f32 v17, v17, v120, v121
	v_max3_f32 v16, v16, v119, v102
	v_max3_f32 v17, v17, v104, v105
	v_max3_f32 v16, v16, v103, v122
	v_max3_f32 v17, v17, v124, v125
	v_max3_f32 v16, v16, v123, v106
	v_max3_f32 v17, v17, v108, v109
	v_max3_f32 v16, v16, v107, v126
	v_max3_f32 v17, v17, v128, v129
	v_max3_f32 v16, v16, v127, v110
	v_max3_f32 v17, v17, v112, v113
	v_max3_f32 v16, v16, v111, v17
	v_mov_b32_e32 v17, v16
	s_nop 1
	v_permlane32_swap_b32_e32 v16, v17
	s_add_i32 s0, s80, s77
	s_mov_b32 m0, s0
	s_nop 0
	global_load_lds_dwordx4 v[210:211], off
	v_max_f32_e32 v16, v16, v17
	s_addk_i32 s0, 0x2000
	s_mov_b32 m0, s0
	s_nop 0
	global_load_lds_dwordx4 v[208:209], off
	v_cmp_lt_f32_e32 vcc, s60, v16
	s_cmp_lg_u64 vcc, 0
	s_cselect_b64 s[0:1], -1, 0
	s_cbranch_vccnz .LBB0_888
.LBB0_883:
	s_waitcnt lgkmcnt(14)
	v_mfma_f32_32x32x16_bf16 v[66:81], v[138:141], v[202:205], v[66:81]
	v_exp_f32_e32 v114, v114
	v_exp_f32_e32 v115, v115
	v_exp_f32_e32 v116, v116
	v_exp_f32_e32 v117, v117
	ds_read_b64_tr_b16 v[166:167], v2 offset:32768
	ds_read_b64_tr_b16 v[168:169], v2 offset:33280
	s_waitcnt lgkmcnt(14)
	v_mfma_f32_32x32x16_bf16 v[50:65], v[138:141], v[198:201], v[50:65]
	v_exp_f32_e32 v118, v118
	v_exp_f32_e32 v119, v119
	v_exp_f32_e32 v120, v120
	v_exp_f32_e32 v121, v121
	ds_read_b64_tr_b16 v[174:175], v2 offset:36864
	ds_read_b64_tr_b16 v[176:177], v2 offset:37376
	s_waitcnt lgkmcnt(14)
	v_mfma_f32_32x32x16_bf16 v[66:81], v[134:137], v[194:197], v[66:81]
	v_exp_f32_e32 v122, v122
	v_exp_f32_e32 v123, v123
	v_exp_f32_e32 v124, v124
	v_exp_f32_e32 v125, v125
	ds_read_b64_tr_b16 v[178:179], v2 offset:33792
	ds_read_b64_tr_b16 v[180:181], v2 offset:34304
	s_waitcnt lgkmcnt(14)
	v_mfma_f32_32x32x16_bf16 v[50:65], v[134:137], v[170:173], v[50:65]
	v_exp_f32_e32 v126, v126
	v_exp_f32_e32 v127, v127
	v_exp_f32_e32 v128, v128
	v_exp_f32_e32 v129, v129
	ds_read_b64_tr_b16 v[182:183], v2 offset:37888
	ds_read_b64_tr_b16 v[184:185], v2 offset:38400
	s_waitcnt lgkmcnt(14)
	v_mfma_f32_32x32x16_bf16 v[66:81], v[130:133], v[162:165], v[66:81]
	v_exp_f32_e32 v98, v98
	v_exp_f32_e32 v99, v99
	v_exp_f32_e32 v100, v100
	v_exp_f32_e32 v101, v101
	ds_read_b64_tr_b16 v[186:187], v2 offset:34816
	ds_read_b64_tr_b16 v[188:189], v2 offset:35328
	s_waitcnt lgkmcnt(14)
	v_mfma_f32_32x32x16_bf16 v[50:65], v[130:133], v[12:15], v[50:65]
	v_exp_f32_e32 v102, v102
	v_exp_f32_e32 v103, v103
	v_exp_f32_e32 v104, v104
	v_exp_f32_e32 v105, v105
	ds_read_b64_tr_b16 v[190:191], v2 offset:38912
	ds_read_b64_tr_b16 v[192:193], v2 offset:39424
	s_waitcnt lgkmcnt(14)
	v_mfma_f32_32x32x16_bf16 v[66:81], v[158:161], v[8:11], v[66:81]
	v_exp_f32_e32 v106, v106
	v_exp_f32_e32 v107, v107
	v_exp_f32_e32 v108, v108
	v_exp_f32_e32 v109, v109
	ds_read_b64_tr_b16 v[194:195], v2 offset:35840
	ds_read_b64_tr_b16 v[196:197], v2 offset:36352
	s_waitcnt lgkmcnt(14)
	v_mfma_f32_32x32x16_bf16 v[50:65], v[158:161], v[4:7], v[50:65]
	v_exp_f32_e32 v110, v110
	v_exp_f32_e32 v111, v111
	v_exp_f32_e32 v112, v112
	v_exp_f32_e32 v113, v113
	ds_read_b64_tr_b16 v[4:5], v2 offset:39936
	ds_read_b64_tr_b16 v[6:7], v2 offset:40448
	v_add_f32_e32 v2, v114, v115
	s_waitcnt lgkmcnt(14)
	v_mfma_f32_32x32x16_bf16 v[34:49], v[138:141], v[166:169], v[34:49]
	v_add_f32_e32 v2, v116, v2
	v_add_f32_e32 v2, v117, v2
	v_add_f32_e32 v2, v118, v2
	v_add_f32_e32 v2, v119, v2
	v_add_u32_e32 v16, s82, v240
	ds_read_b128 v[12:15], v16
	ds_read_b128 v[8:11], v16 offset:512
	s_waitcnt lgkmcnt(14)
	v_mfma_f32_32x32x16_bf16 v[18:33], v[138:141], v[174:177], v[18:33]
	v_add_f32_e32 v2, v120, v2
	v_add_f32_e32 v2, v121, v2
	v_add_f32_e32 v2, v122, v2
	v_add_f32_e32 v2, v123, v2
	ds_read_b128 v[166:169], v16 offset:2048
	ds_read_b128 v[162:165], v16 offset:2560
	s_waitcnt lgkmcnt(14)
	v_mfma_f32_32x32x16_bf16 v[34:49], v[134:137], v[178:181], v[34:49]
	v_add_f32_e32 v2, v124, v2
	v_add_f32_e32 v2, v125, v2
	v_add_f32_e32 v2, v126, v2
	v_add_f32_e32 v2, v127, v2
	v_cvt_pk_bf16_f32 v138, v114, v115
	v_cvt_pk_bf16_f32 v139, v116, v117
	ds_read_b128 v[174:177], v16 offset:4096
	ds_read_b128 v[170:173], v16 offset:4608
	s_waitcnt lgkmcnt(14)
	v_mfma_f32_32x32x16_bf16 v[18:33], v[134:137], v[182:185], v[18:33]
	v_add_f32_e32 v2, v128, v2
	v_add_f32_e32 v2, v129, v2
	v_add_f32_e32 v2, v98, v2
	v_add_f32_e32 v2, v99, v2
	v_cvt_pk_bf16_f32 v140, v118, v119
	v_cvt_pk_bf16_f32 v141, v120, v121
	ds_read_b128 v[182:185], v16 offset:6144
	ds_read_b128 v[178:181], v16 offset:6656
	s_waitcnt lgkmcnt(14)
	v_mfma_f32_32x32x16_bf16 v[34:49], v[130:133], v[186:189], v[34:49]
	v_add_f32_e32 v2, v100, v2
	v_add_f32_e32 v2, v101, v2
	v_add_f32_e32 v2, v102, v2
	v_add_f32_e32 v2, v103, v2
	v_cvt_pk_bf16_f32 v134, v122, v123
	v_cvt_pk_bf16_f32 v135, v124, v125
	s_waitcnt lgkmcnt(12)
	v_mfma_f32_32x32x16_bf16 v[18:33], v[130:133], v[190:193], v[18:33]
	v_add_f32_e32 v2, v104, v2
	v_add_f32_e32 v2, v105, v2
	v_add_f32_e32 v2, v106, v2
	v_add_f32_e32 v2, v107, v2
	v_cvt_pk_bf16_f32 v136, v126, v127
	v_cvt_pk_bf16_f32 v137, v128, v129
	s_waitcnt lgkmcnt(10)
	v_mfma_f32_32x32x16_bf16 v[34:49], v[158:161], v[194:197], v[34:49]
	v_add_f32_e32 v2, v108, v2
	v_add_f32_e32 v2, v109, v2
	v_add_f32_e32 v2, v110, v2
	v_add_f32_e32 v2, v111, v2
	v_cvt_pk_bf16_f32 v130, v98, v99
	v_cvt_pk_bf16_f32 v131, v100, v101
	s_waitcnt lgkmcnt(8)
	v_mfma_f32_32x32x16_bf16 v[18:33], v[158:161], v[4:7], v[18:33]
	v_add_f32_e32 v2, v112, v2
	v_add_f32_e32 v2, v113, v2
	v_cvt_pk_bf16_f32 v132, v102, v103
	v_cvt_pk_bf16_f32 v133, v104, v105
	v_cvt_pk_bf16_f32 v4, v106, v107
	v_cvt_pk_bf16_f32 v5, v108, v109
	v_cvt_pk_bf16_f32 v6, v110, v111
	v_cvt_pk_bf16_f32 v7, v112, v113
	s_waitcnt vmcnt(3) lgkmcnt(0)
	s_barrier
	s_andn2_b64 vcc, exec, s[0:1]
	s_cbranch_vccnz .LBB0_885
	s_waitcnt lgkmcnt(0)
	ds_read2_b32 v[16:17], v234 offset1:1
	ds_read2_b32 v[98:99], v234 offset0:2 offset1:3
	ds_read2_b32 v[100:101], v234 offset0:8 offset1:9
	ds_read2_b32 v[102:103], v234 offset0:10 offset1:11
	s_waitcnt lgkmcnt(3)
	v_mul_f32_e32 v66, v66, v16
	v_mul_f32_e32 v50, v50, v16
	v_mul_f32_e32 v34, v34, v16
	v_mul_f32_e32 v18, v18, v16
	v_mul_f32_e32 v67, v67, v17
	v_mul_f32_e32 v51, v51, v17
	v_mul_f32_e32 v35, v35, v17
	v_mul_f32_e32 v19, v19, v17
	s_waitcnt lgkmcnt(2)
	v_mul_f32_e32 v68, v68, v98
	v_mul_f32_e32 v52, v52, v98
	v_mul_f32_e32 v36, v36, v98
	v_mul_f32_e32 v20, v20, v98
	v_mul_f32_e32 v69, v69, v99
	v_mul_f32_e32 v53, v53, v99
	v_mul_f32_e32 v37, v37, v99
	v_mul_f32_e32 v21, v21, v99
	s_waitcnt lgkmcnt(1)
	v_mul_f32_e32 v70, v70, v100
	v_mul_f32_e32 v54, v54, v100
	v_mul_f32_e32 v38, v38, v100
	v_mul_f32_e32 v22, v22, v100
	v_mul_f32_e32 v71, v71, v101
	v_mul_f32_e32 v55, v55, v101
	v_mul_f32_e32 v39, v39, v101
	v_mul_f32_e32 v23, v23, v101
	s_waitcnt lgkmcnt(0)
	v_mul_f32_e32 v72, v72, v102
	v_mul_f32_e32 v56, v56, v102
	v_mul_f32_e32 v40, v40, v102
	v_mul_f32_e32 v24, v24, v102
	v_mul_f32_e32 v73, v73, v103
	v_mul_f32_e32 v57, v57, v103
	v_mul_f32_e32 v41, v41, v103
	ds_read2_b32 v[16:17], v234 offset0:16 offset1:17
	v_mul_f32_e32 v25, v25, v103
	ds_read2_b32 v[98:99], v234 offset0:18 offset1:19
	ds_read2_b32 v[100:101], v234 offset0:24 offset1:25
	ds_read2_b32 v[102:103], v234 offset0:26 offset1:27
	s_waitcnt lgkmcnt(3)
	v_mul_f32_e32 v74, v74, v16
	v_mul_f32_e32 v58, v58, v16
	v_mul_f32_e32 v42, v42, v16
	v_mul_f32_e32 v26, v26, v16
	v_mul_f32_e32 v75, v75, v17
	v_mul_f32_e32 v59, v59, v17
	v_mul_f32_e32 v43, v43, v17
	v_mul_f32_e32 v27, v27, v17
	s_waitcnt lgkmcnt(2)
	v_mul_f32_e32 v76, v76, v98
	v_mul_f32_e32 v60, v60, v98
	v_mul_f32_e32 v44, v44, v98
	v_mul_f32_e32 v28, v28, v98
	v_mul_f32_e32 v77, v77, v99
	v_mul_f32_e32 v61, v61, v99
	v_mul_f32_e32 v45, v45, v99
	v_mul_f32_e32 v29, v29, v99
	s_waitcnt lgkmcnt(1)
	v_mul_f32_e32 v78, v78, v100
	v_mul_f32_e32 v62, v62, v100
	v_mul_f32_e32 v46, v46, v100
	v_mul_f32_e32 v30, v30, v100
	v_mul_f32_e32 v79, v79, v101
	v_mul_f32_e32 v63, v63, v101
	v_mul_f32_e32 v47, v47, v101
	v_mul_f32_e32 v31, v31, v101
	s_waitcnt lgkmcnt(0)
	v_mul_f32_e32 v80, v80, v102
	v_mul_f32_e32 v64, v64, v102
	v_mul_f32_e32 v48, v48, v102
	v_mul_f32_e32 v32, v32, v102
	v_mul_f32_e32 v81, v81, v103
	v_mul_f32_e32 v65, v65, v103
	v_mul_f32_e32 v49, v49, v103
	v_mul_f32_e32 v33, v33, v103
.LBB0_885:
	s_add_i32 s0, s43, 0x4000
	s_add_i32 s1, s80, 0x4000
	v_add_f32_e32 v2, v243, v2
	s_and_b32 s0, s0, 0xffff
	s_and_b32 s1, s1, 0xffff
	v_add_u32_e32 v16, s0, v242
	ds_read_b64_tr_b16 v[194:195], v16 offset:24576
	ds_read_b64_tr_b16 v[196:197], v16 offset:25088
	s_waitcnt lgkmcnt(9)
	v_mfma_f32_32x32x16_bf16 v[114:129], v[12:15], v[154:157], v[82:97]
	ds_read_b64_tr_b16 v[190:191], v16 offset:28672
	ds_read_b64_tr_b16 v[192:193], v16 offset:29184
	s_waitcnt lgkmcnt(10)
	v_mfma_f32_32x32x16_bf16 v[98:113], v[8:11], v[154:157], v[82:97]
	ds_read_b64_tr_b16 v[186:187], v16 offset:25600
	ds_read_b64_tr_b16 v[188:189], v16 offset:26112
	s_waitcnt lgkmcnt(11)
	v_mfma_f32_32x32x16_bf16 v[114:129], v[166:169], v[150:153], v[114:129]
	ds_read_b64_tr_b16 v[166:167], v16 offset:29696
	ds_read_b64_tr_b16 v[168:169], v16 offset:30208
	s_waitcnt lgkmcnt(12)
	v_mfma_f32_32x32x16_bf16 v[98:113], v[162:165], v[150:153], v[98:113]
	ds_read_b64_tr_b16 v[162:163], v16 offset:26624
	ds_read_b64_tr_b16 v[164:165], v16 offset:27136
	s_waitcnt lgkmcnt(13)
	v_mfma_f32_32x32x16_bf16 v[114:129], v[174:177], v[146:149], v[114:129]
	ds_read_b64_tr_b16 v[158:159], v16 offset:30720
	ds_read_b64_tr_b16 v[160:161], v16 offset:31232
	s_waitcnt lgkmcnt(14)
	v_mfma_f32_32x32x16_bf16 v[98:113], v[170:173], v[146:149], v[98:113]
	ds_read_b64_tr_b16 v[12:13], v16 offset:27648
	ds_read_b64_tr_b16 v[14:15], v16 offset:28160
	s_waitcnt lgkmcnt(14)
	v_mfma_f32_32x32x16_bf16 v[114:129], v[182:185], v[142:145], v[114:129]
	ds_read_b64_tr_b16 v[8:9], v16 offset:31744
	ds_read_b64_tr_b16 v[10:11], v16 offset:32256
	v_mfma_f32_32x32x16_bf16 v[98:113], v[178:181], v[142:145], v[98:113]
	s_add_i32 s0, s82, s76
	s_mov_b32 m0, s0
	s_nop 0
	global_load_lds_dwordx4 v[206:207], off
	v_lshl_add_u64 v[170:171], v[210:211], 0, s[18:19]
	s_add_i32 s0, s1, s77
	s_mov_b32 m0, s0
	s_nop 0
	global_load_lds_dwordx4 v[170:171], off
	v_lshl_add_u64 v[170:171], v[208:209], 0, s[18:19]
	s_addk_i32 s0, 0x2000
	s_mov_b32 m0, s0
	s_nop 0
	global_load_lds_dwordx4 v[170:171], off
	s_nop 3
	v_max_f32_e32 v17, v115, v114
	v_max3_f32 v170, v116, v117, v99
	v_max3_f32 v17, v17, v98, v100
	v_max3_f32 v17, v17, v101, v118
	v_max3_f32 v170, v170, v120, v121
	v_max3_f32 v17, v17, v119, v102
	v_max3_f32 v170, v170, v104, v105
	v_max3_f32 v17, v17, v103, v122
	v_max3_f32 v170, v170, v124, v125
	v_max3_f32 v17, v17, v123, v106
	v_max3_f32 v170, v170, v108, v109
	v_max3_f32 v17, v17, v107, v126
	v_max3_f32 v170, v170, v128, v129
	v_max3_f32 v17, v17, v127, v110
	v_max3_f32 v170, v170, v112, v113
	v_max3_f32 v17, v17, v111, v170
	v_mov_b32_e32 v170, v17
	s_nop 1
	v_permlane32_swap_b32_e32 v17, v170
	v_max_f32_e32 v17, v17, v170
	v_cmp_lt_f32_e32 vcc, s60, v17
	s_cmp_lg_u64 vcc, 0
	s_cselect_b64 s[0:1], -1, 0
	s_cbranch_vccnz .LBB0_891
.LBB0_886:
	s_add_i32 s28, s82, 0x2000
	s_cmpk_lg_i32 s82, 0x4000
	s_cselect_b32 s38, s28, 0
	s_waitcnt lgkmcnt(14)
	v_mfma_f32_32x32x16_bf16 v[66:81], v[138:141], v[194:197], v[66:81]
	v_exp_f32_e32 v114, v114
	v_exp_f32_e32 v115, v115
	v_exp_f32_e32 v116, v116
	v_exp_f32_e32 v117, v117
	ds_read_b64_tr_b16 v[170:171], v16 offset:32768
	ds_read_b64_tr_b16 v[172:173], v16 offset:33280
	s_waitcnt lgkmcnt(14)
	v_mfma_f32_32x32x16_bf16 v[50:65], v[138:141], v[190:193], v[50:65]
	v_exp_f32_e32 v118, v118
	v_exp_f32_e32 v119, v119
	v_exp_f32_e32 v120, v120
	v_exp_f32_e32 v121, v121
	ds_read_b64_tr_b16 v[174:175], v16 offset:36864
	ds_read_b64_tr_b16 v[176:177], v16 offset:37376
	s_waitcnt lgkmcnt(14)
	v_mfma_f32_32x32x16_bf16 v[66:81], v[134:137], v[186:189], v[66:81]
	v_exp_f32_e32 v122, v122
	v_exp_f32_e32 v123, v123
	v_exp_f32_e32 v124, v124
	v_exp_f32_e32 v125, v125
	ds_read_b64_tr_b16 v[178:179], v16 offset:33792
	ds_read_b64_tr_b16 v[180:181], v16 offset:34304
	s_waitcnt lgkmcnt(14)
	v_mfma_f32_32x32x16_bf16 v[50:65], v[134:137], v[166:169], v[50:65]
	v_exp_f32_e32 v126, v126
	v_exp_f32_e32 v127, v127
	v_exp_f32_e32 v128, v128
	v_exp_f32_e32 v129, v129
	ds_read_b64_tr_b16 v[186:187], v16 offset:37888
	ds_read_b64_tr_b16 v[188:189], v16 offset:38400
	s_waitcnt lgkmcnt(14)
	v_mfma_f32_32x32x16_bf16 v[66:81], v[130:133], v[162:165], v[66:81]
	v_exp_f32_e32 v98, v98
	v_exp_f32_e32 v99, v99
	v_exp_f32_e32 v100, v100
	v_exp_f32_e32 v101, v101
	ds_read_b64_tr_b16 v[194:195], v16 offset:34816
	ds_read_b64_tr_b16 v[196:197], v16 offset:35328
	s_waitcnt lgkmcnt(14)
	v_mfma_f32_32x32x16_bf16 v[50:65], v[130:133], v[158:161], v[50:65]
	v_exp_f32_e32 v102, v102
	v_exp_f32_e32 v103, v103
	v_exp_f32_e32 v104, v104
	v_exp_f32_e32 v105, v105
	ds_read_b64_tr_b16 v[158:159], v16 offset:38912
	ds_read_b64_tr_b16 v[160:161], v16 offset:39424
	s_waitcnt lgkmcnt(14)
	v_mfma_f32_32x32x16_bf16 v[66:81], v[4:7], v[12:15], v[66:81]
	v_exp_f32_e32 v106, v106
	v_exp_f32_e32 v107, v107
	v_exp_f32_e32 v108, v108
	v_exp_f32_e32 v109, v109
	ds_read_b64_tr_b16 v[12:13], v16 offset:35840
	ds_read_b64_tr_b16 v[14:15], v16 offset:36352
	s_waitcnt lgkmcnt(14)
	v_mfma_f32_32x32x16_bf16 v[50:65], v[4:7], v[8:11], v[50:65]
	v_exp_f32_e32 v110, v110
	v_exp_f32_e32 v111, v111
	v_exp_f32_e32 v112, v112
	v_exp_f32_e32 v113, v113
	ds_read_b64_tr_b16 v[198:199], v16 offset:39936
	ds_read_b64_tr_b16 v[200:201], v16 offset:40448
	v_add_f32_e32 v8, v114, v115
	s_waitcnt lgkmcnt(14)
	v_mfma_f32_32x32x16_bf16 v[34:49], v[138:141], v[170:173], v[34:49]
	v_add_f32_e32 v8, v116, v8
	v_add_f32_e32 v8, v117, v8
	v_add_f32_e32 v8, v118, v8
	v_add_f32_e32 v8, v119, v8
	v_add_u32_e32 v9, s38, v240
	ds_read_b128 v[170:173], v9
	ds_read_b128 v[162:165], v9 offset:512
	s_waitcnt lgkmcnt(14)
	v_mfma_f32_32x32x16_bf16 v[18:33], v[138:141], v[174:177], v[18:33]
	v_add_f32_e32 v8, v120, v8
	v_add_f32_e32 v8, v121, v8
	v_add_f32_e32 v8, v122, v8
	v_add_f32_e32 v8, v123, v8
	ds_read_b128 v[174:177], v9 offset:2048
	ds_read_b128 v[166:169], v9 offset:2560
	s_waitcnt lgkmcnt(14)
	v_mfma_f32_32x32x16_bf16 v[34:49], v[134:137], v[178:181], v[34:49]
	v_add_f32_e32 v8, v124, v8
	v_add_f32_e32 v8, v125, v8
	v_add_f32_e32 v8, v126, v8
	v_add_f32_e32 v8, v127, v8
	v_cvt_pk_bf16_f32 v138, v114, v115
	v_cvt_pk_bf16_f32 v139, v116, v117
	ds_read_b128 v[182:185], v9 offset:4096
	ds_read_b128 v[178:181], v9 offset:4608
	s_waitcnt lgkmcnt(14)
	v_mfma_f32_32x32x16_bf16 v[18:33], v[134:137], v[186:189], v[18:33]
	v_add_f32_e32 v8, v128, v8
	v_add_f32_e32 v8, v129, v8
	v_add_f32_e32 v8, v98, v8
	v_add_f32_e32 v8, v99, v8
	v_cvt_pk_bf16_f32 v140, v118, v119
	v_cvt_pk_bf16_f32 v141, v120, v121
	ds_read_b128 v[190:193], v9 offset:6144
	ds_read_b128 v[186:189], v9 offset:6656
	s_waitcnt lgkmcnt(14)
	v_mfma_f32_32x32x16_bf16 v[34:49], v[130:133], v[194:197], v[34:49]
	v_add_f32_e32 v8, v100, v8
	v_add_f32_e32 v8, v101, v8
	v_add_f32_e32 v8, v102, v8
	v_add_f32_e32 v8, v103, v8
	v_cvt_pk_bf16_f32 v134, v122, v123
	v_cvt_pk_bf16_f32 v135, v124, v125
	s_waitcnt lgkmcnt(12)
	v_mfma_f32_32x32x16_bf16 v[18:33], v[130:133], v[158:161], v[18:33]
	v_add_f32_e32 v8, v104, v8
	v_add_f32_e32 v8, v105, v8
	v_add_f32_e32 v8, v106, v8
	v_add_f32_e32 v8, v107, v8
	v_cvt_pk_bf16_f32 v136, v126, v127
	v_cvt_pk_bf16_f32 v137, v128, v129
	s_waitcnt lgkmcnt(10)
	v_mfma_f32_32x32x16_bf16 v[34:49], v[4:7], v[12:15], v[34:49]
	v_add_f32_e32 v8, v108, v8
	v_add_f32_e32 v8, v109, v8
	v_add_f32_e32 v8, v110, v8
	v_add_f32_e32 v8, v111, v8
	v_cvt_pk_bf16_f32 v130, v98, v99
	v_cvt_pk_bf16_f32 v131, v100, v101
	s_waitcnt lgkmcnt(8)
	v_mfma_f32_32x32x16_bf16 v[18:33], v[4:7], v[198:201], v[18:33]
	v_add_f32_e32 v8, v112, v8
	v_add_f32_e32 v8, v113, v8
	v_cvt_pk_bf16_f32 v132, v102, v103
	v_cvt_pk_bf16_f32 v133, v104, v105
	v_cvt_pk_bf16_f32 v158, v106, v107
	v_cvt_pk_bf16_f32 v159, v108, v109
	v_cvt_pk_bf16_f32 v160, v110, v111
	v_cvt_pk_bf16_f32 v161, v112, v113
	s_waitcnt vmcnt(3) lgkmcnt(0)
	s_barrier
	s_andn2_b64 vcc, exec, s[0:1]
	s_cbranch_vccnz .LBB0_881
	s_waitcnt lgkmcnt(0)
	ds_read2_b32 v[4:5], v234 offset1:1
	ds_read2_b32 v[6:7], v234 offset0:2 offset1:3
	ds_read2_b32 v[10:11], v234 offset0:8 offset1:9
	ds_read2_b32 v[12:13], v234 offset0:10 offset1:11
	s_waitcnt lgkmcnt(3)
	v_mul_f32_e32 v66, v66, v4
	v_mul_f32_e32 v50, v50, v4
	v_mul_f32_e32 v34, v34, v4
	v_mul_f32_e32 v18, v18, v4
	v_mul_f32_e32 v67, v67, v5
	v_mul_f32_e32 v51, v51, v5
	v_mul_f32_e32 v35, v35, v5
	v_mul_f32_e32 v19, v19, v5
	s_waitcnt lgkmcnt(2)
	v_mul_f32_e32 v68, v68, v6
	v_mul_f32_e32 v52, v52, v6
	v_mul_f32_e32 v36, v36, v6
	v_mul_f32_e32 v20, v20, v6
	v_mul_f32_e32 v69, v69, v7
	v_mul_f32_e32 v53, v53, v7
	v_mul_f32_e32 v37, v37, v7
	v_mul_f32_e32 v21, v21, v7
	s_waitcnt lgkmcnt(1)
	v_mul_f32_e32 v70, v70, v10
	v_mul_f32_e32 v54, v54, v10
	v_mul_f32_e32 v38, v38, v10
	v_mul_f32_e32 v22, v22, v10
	v_mul_f32_e32 v71, v71, v11
	v_mul_f32_e32 v55, v55, v11
	v_mul_f32_e32 v39, v39, v11
	v_mul_f32_e32 v23, v23, v11
	s_waitcnt lgkmcnt(0)
	v_mul_f32_e32 v72, v72, v12
	v_mul_f32_e32 v56, v56, v12
	v_mul_f32_e32 v40, v40, v12
	v_mul_f32_e32 v24, v24, v12
	v_mul_f32_e32 v73, v73, v13
	v_mul_f32_e32 v57, v57, v13
	v_mul_f32_e32 v41, v41, v13
	ds_read2_b32 v[4:5], v234 offset0:16 offset1:17
	v_mul_f32_e32 v25, v25, v13
	ds_read2_b32 v[6:7], v234 offset0:18 offset1:19
	ds_read2_b32 v[10:11], v234 offset0:24 offset1:25
	ds_read2_b32 v[12:13], v234 offset0:26 offset1:27
	s_waitcnt lgkmcnt(3)
	v_mul_f32_e32 v74, v74, v4
	v_mul_f32_e32 v58, v58, v4
	v_mul_f32_e32 v42, v42, v4
	v_mul_f32_e32 v26, v26, v4
	v_mul_f32_e32 v75, v75, v5
	v_mul_f32_e32 v59, v59, v5
	v_mul_f32_e32 v43, v43, v5
	v_mul_f32_e32 v27, v27, v5
	s_waitcnt lgkmcnt(2)
	v_mul_f32_e32 v76, v76, v6
	v_mul_f32_e32 v60, v60, v6
	v_mul_f32_e32 v44, v44, v6
	v_mul_f32_e32 v28, v28, v6
	v_mul_f32_e32 v77, v77, v7
	v_mul_f32_e32 v61, v61, v7
	v_mul_f32_e32 v45, v45, v7
	v_mul_f32_e32 v29, v29, v7
	s_waitcnt lgkmcnt(1)
	v_mul_f32_e32 v78, v78, v10
	v_mul_f32_e32 v62, v62, v10
	v_mul_f32_e32 v46, v46, v10
	v_mul_f32_e32 v30, v30, v10
	v_mul_f32_e32 v79, v79, v11
	v_mul_f32_e32 v63, v63, v11
	v_mul_f32_e32 v47, v47, v11
	v_mul_f32_e32 v31, v31, v11
	s_waitcnt lgkmcnt(0)
	v_mul_f32_e32 v80, v80, v12
	v_mul_f32_e32 v64, v64, v12
	v_mul_f32_e32 v48, v48, v12
	v_mul_f32_e32 v32, v32, v12
	v_mul_f32_e32 v81, v81, v13
	v_mul_f32_e32 v65, v65, v13
	v_mul_f32_e32 v49, v49, v13
	v_mul_f32_e32 v33, v33, v13
	s_branch .LBB0_881

.LBB0_897:
	v_add_u32_e32 v206, s43, v242
	ds_read_b64_tr_b16 v[202:203], v206 offset:24576
	ds_read_b64_tr_b16 v[204:205], v206 offset:25088
	s_waitcnt lgkmcnt(9)
	v_mfma_f32_32x32x16_bf16 v[114:129], v[170:173], v[154:157], v[82:97]
	ds_read_b64_tr_b16 v[198:199], v206 offset:28672
	ds_read_b64_tr_b16 v[200:201], v206 offset:29184
	s_waitcnt lgkmcnt(10)
	v_mfma_f32_32x32x16_bf16 v[98:113], v[162:165], v[154:157], v[82:97]
	ds_read_b64_tr_b16 v[194:195], v206 offset:25600
	ds_read_b64_tr_b16 v[196:197], v206 offset:26112
	s_waitcnt lgkmcnt(11)
	v_mfma_f32_32x32x16_bf16 v[114:129], v[174:177], v[150:153], v[114:129]
	ds_read_b64_tr_b16 v[170:171], v206 offset:29696
	ds_read_b64_tr_b16 v[172:173], v206 offset:30208
	s_waitcnt lgkmcnt(12)
	v_mfma_f32_32x32x16_bf16 v[98:113], v[166:169], v[150:153], v[98:113]
	ds_read_b64_tr_b16 v[162:163], v206 offset:26624
	ds_read_b64_tr_b16 v[164:165], v206 offset:27136
	s_waitcnt lgkmcnt(13)
	v_mfma_f32_32x32x16_bf16 v[114:129], v[182:185], v[146:149], v[114:129]
	ds_read_b64_tr_b16 v[12:13], v206 offset:30720
	ds_read_b64_tr_b16 v[14:15], v206 offset:31232
	s_waitcnt lgkmcnt(14)
	v_mfma_f32_32x32x16_bf16 v[98:113], v[178:181], v[146:149], v[98:113]
	ds_read_b64_tr_b16 v[8:9], v206 offset:27648
	ds_read_b64_tr_b16 v[10:11], v206 offset:28160
	s_waitcnt lgkmcnt(14)
	v_mfma_f32_32x32x16_bf16 v[114:129], v[190:193], v[142:145], v[114:129]
	ds_read_b64_tr_b16 v[4:5], v206 offset:31744
	ds_read_b64_tr_b16 v[6:7], v206 offset:32256
	v_mfma_f32_32x32x16_bf16 v[98:113], v[186:189], v[142:145], v[98:113]
	s_add_i32 s30, s81, 3
	s_cmp_lt_i32 s30, s79
	s_cselect_b64 s[0:1], -1, 0
	s_cmp_ge_i32 s30, s79
	s_cselect_b64 s[30:31], -1, 0
	s_and_b64 vcc, exec, s[30:31]
	v_lshl_add_u64 v[16:17], v[216:217], 0, s[28:29]
	s_cbranch_vccnz .LBB0_899
	v_lshl_add_u64 v[166:167], v[16:17], 0, s[24:25]
	s_add_i32 s34, s38, s76
	s_mov_b32 m0, s34
	s_nop 0
	global_load_lds_dwordx4 v[166:167], off
.LBB0_899:
	s_add_i32 s74, s81, 2
	s_cmp_lt_i32 s74, s79
	s_cselect_b64 s[34:35], -1, 0
	s_cmp_ge_i32 s74, s79
	s_cselect_b64 s[36:37], -1, 0
	s_and_b64 vcc, exec, s[36:37]
	v_lshl_add_u64 v[224:225], v[218:219], 0, s[28:29]
	v_lshl_add_u64 v[222:223], v[220:221], 0, s[28:29]
	s_cbranch_vccnz .LBB0_901
	v_lshl_add_u64 v[166:167], v[224:225], 0, s[22:23]
	s_add_i32 s38, s80, s77
	s_mov_b32 m0, s38
	s_nop 0
	global_load_lds_dwordx4 v[166:167], off
	v_lshl_add_u64 v[166:167], v[222:223], 0, s[22:23]
	s_addk_i32 s38, 0x2000
	s_mov_b32 m0, s38
	s_nop 0
	global_load_lds_dwordx4 v[166:167], off

.LBB0_905:
	s_nop 0
	v_max_f32_e32 v166, v115, v114
	v_max3_f32 v167, v116, v117, v99
	v_max3_f32 v166, v166, v98, v100
	v_max3_f32 v166, v166, v101, v118
	v_max3_f32 v167, v167, v120, v121
	v_max3_f32 v166, v166, v119, v102
	v_max3_f32 v167, v167, v104, v105
	v_max3_f32 v166, v166, v103, v122
	v_max3_f32 v167, v167, v124, v125
	v_max3_f32 v166, v166, v123, v106
	v_max3_f32 v167, v167, v108, v109
	v_max3_f32 v166, v166, v107, v126
	v_max3_f32 v167, v167, v128, v129
	v_max3_f32 v166, v166, v127, v110
	v_max3_f32 v167, v167, v112, v113
	v_max3_f32 v166, v166, v111, v167
	v_mov_b32_e32 v167, v166
	s_nop 1
	v_permlane32_swap_b32_e32 v166, v167
	v_max_f32_e32 v166, v166, v167
	v_cmp_lt_f32_e32 vcc, s60, v166
	s_cmp_lg_u64 vcc, 0
	s_cselect_b64 s[44:45], -1, 0
	s_cbranch_vccnz .LBB0_945

.LBB0_914:
	s_add_i32 s36, s43, 0x4000
	s_and_b32 s36, s36, 0xffff
	v_add_u32_e32 v249, s36, v242
	ds_read_b64_tr_b16 v[210:211], v249 offset:24576
	ds_read_b64_tr_b16 v[212:213], v249 offset:25088
	s_waitcnt lgkmcnt(9)
	v_mfma_f32_32x32x16_bf16 v[114:129], v[170:173], v[154:157], v[82:97]
	ds_read_b64_tr_b16 v[206:207], v249 offset:28672
	ds_read_b64_tr_b16 v[208:209], v249 offset:29184
	s_waitcnt lgkmcnt(10)
	v_mfma_f32_32x32x16_bf16 v[98:113], v[162:165], v[154:157], v[82:97]
	ds_read_b64_tr_b16 v[202:203], v249 offset:25600
	ds_read_b64_tr_b16 v[204:205], v249 offset:26112
	s_waitcnt lgkmcnt(11)
	v_mfma_f32_32x32x16_bf16 v[114:129], v[174:177], v[150:153], v[114:129]
	ds_read_b64_tr_b16 v[198:199], v249 offset:29696
	ds_read_b64_tr_b16 v[200:201], v249 offset:30208
	s_waitcnt lgkmcnt(12)
	v_mfma_f32_32x32x16_bf16 v[98:113], v[166:169], v[150:153], v[98:113]
	ds_read_b64_tr_b16 v[194:195], v249 offset:26624
	ds_read_b64_tr_b16 v[196:197], v249 offset:27136
	s_waitcnt lgkmcnt(13)
	v_mfma_f32_32x32x16_bf16 v[114:129], v[182:185], v[146:149], v[114:129]
	ds_read_b64_tr_b16 v[158:159], v249 offset:30720
	ds_read_b64_tr_b16 v[160:161], v249 offset:31232
	s_waitcnt lgkmcnt(14)
	v_mfma_f32_32x32x16_bf16 v[98:113], v[178:181], v[146:149], v[98:113]
	ds_read_b64_tr_b16 v[12:13], v249 offset:27648
	ds_read_b64_tr_b16 v[14:15], v249 offset:28160
	s_waitcnt lgkmcnt(14)
	v_mfma_f32_32x32x16_bf16 v[114:129], v[190:193], v[142:145], v[114:129]
	ds_read_b64_tr_b16 v[8:9], v249 offset:31744
	ds_read_b64_tr_b16 v[10:11], v249 offset:32256
	v_mfma_f32_32x32x16_bf16 v[98:113], v[186:189], v[142:145], v[98:113]
	s_add_i32 s36, s81, 4
	s_cmp_ge_i32 s36, s79
	s_cselect_b64 s[36:37], -1, 0
	s_and_b64 vcc, exec, s[36:37]
	s_cbranch_vccnz .LBB0_941
	s_mov_b64 s[38:39], 0x120000
	v_lshl_add_u64 v[16:17], v[16:17], 0, s[38:39]
	s_add_i32 s38, s82, s76
	s_mov_b32 m0, s38
	s_nop 0
	global_load_lds_dwordx4 v[16:17], off
	s_andn2_b64 vcc, exec, s[0:1]
	s_cbranch_vccz .LBB0_942

.LBB0_920:
	s_nop 0
	v_max_f32_e32 v17, v115, v114
	v_max3_f32 v222, v116, v117, v99
	v_max3_f32 v17, v17, v98, v100
	v_max3_f32 v17, v17, v101, v118
	v_max3_f32 v222, v222, v120, v121
	v_max3_f32 v17, v17, v119, v102
	v_max3_f32 v222, v222, v104, v105
	v_max3_f32 v17, v17, v103, v122
	v_max3_f32 v222, v222, v124, v125
	v_max3_f32 v17, v17, v123, v106
	v_max3_f32 v222, v222, v108, v109
	v_max3_f32 v17, v17, v107, v126
	v_max3_f32 v222, v222, v128, v129
	v_max3_f32 v17, v17, v127, v110
	v_max3_f32 v222, v222, v112, v113
	v_max3_f32 v17, v17, v111, v222
	v_mov_b32_e32 v222, v17
	s_nop 1
	v_permlane32_swap_b32_e32 v17, v222
	v_max_f32_e32 v17, v17, v222
	v_cmp_lt_f32_e32 vcc, s60, v17
	s_cmp_lg_u64 vcc, 0
	v_add_f32_e32 v16, v243, v248
	s_cselect_b64 s[44:45], -1, 0
	s_cbranch_vccnz .LBB0_948

.LBB0_929:
	s_waitcnt lgkmcnt(6)
	v_mfma_f32_32x32x16_bf16 v[34:49], v[130:133], v[194:197], v[34:49]
	v_add_f32_e32 v17, v100, v114
	v_add_f32_e32 v17, v101, v17
	v_add_f32_e32 v17, v102, v17
	v_add_f32_e32 v17, v103, v17
	v_cvt_pk_bf16_f32 v134, v122, v123
	v_cvt_pk_bf16_f32 v135, v124, v125
	s_waitcnt lgkmcnt(4)
	v_mfma_f32_32x32x16_bf16 v[18:33], v[130:133], v[158:161], v[18:33]
	v_add_f32_e32 v17, v104, v17
	v_add_f32_e32 v17, v105, v17
	v_add_f32_e32 v17, v106, v17
	v_add_f32_e32 v17, v107, v17
	v_cvt_pk_bf16_f32 v136, v126, v127
	v_cvt_pk_bf16_f32 v137, v128, v129
	s_waitcnt lgkmcnt(2)
	v_mfma_f32_32x32x16_bf16 v[34:49], v[4:7], v[12:15], v[34:49]
	v_add_f32_e32 v17, v108, v17
	v_add_f32_e32 v17, v109, v17
	v_add_f32_e32 v17, v110, v17
	v_add_f32_e32 v17, v111, v17
	v_cvt_pk_bf16_f32 v130, v98, v99
	v_cvt_pk_bf16_f32 v131, v100, v101
	s_waitcnt lgkmcnt(0)
	v_mfma_f32_32x32x16_bf16 v[18:33], v[4:7], v[8:11], v[18:33]
	v_add_f32_e32 v12, v112, v17
	v_add_f32_e32 v12, v113, v12
	v_cvt_pk_bf16_f32 v132, v102, v103
	v_cvt_pk_bf16_f32 v133, v104, v105
	v_cvt_pk_bf16_f32 v158, v106, v107
	v_cvt_pk_bf16_f32 v159, v108, v109
	v_cvt_pk_bf16_f32 v160, v110, v111
	v_cvt_pk_bf16_f32 v161, v112, v113
	s_mov_b64 s[0:1], -1
	s_and_b64 vcc, exec, s[36:37]
	s_cbranch_vccz .LBB0_943
	s_and_b64 vcc, exec, s[30:31]
	s_cbranch_vccz .LBB0_932
	s_waitcnt vmcnt(0) lgkmcnt(0)
	s_barrier
	s_mov_b64 s[0:1], 0

.LBB0_942:
	s_add_i32 s0, s80, 0x4000
	s_and_b32 s0, s0, 0xffff
	v_lshl_add_u64 v[16:17], v[224:225], 0, s[24:25]
	s_add_i32 s0, s0, s77
	s_mov_b32 m0, s0
	s_nop 0
	global_load_lds_dwordx4 v[16:17], off
	v_lshl_add_u64 v[16:17], v[222:223], 0, s[24:25]
	s_addk_i32 s0, 0x2000
	s_mov_b32 m0, s0
	s_nop 0
	global_load_lds_dwordx4 v[16:17], off
	s_add_i32 s75, s75, 5
	s_cmp_lt_i32 s75, 0
	s_cbranch_scc0 .LBB0_917
	s_branch .LBB0_918

.LBB0_952:
	v_add_u32_e32 v2, s43, v242
	ds_read_b64_tr_b16 v[194:195], v2 offset:24576
	ds_read_b64_tr_b16 v[196:197], v2 offset:25088
	s_waitcnt lgkmcnt(9)
	v_mfma_f32_32x32x16_bf16 v[82:97], v[170:173], v[154:157], v[100:115]
	ds_read_b64_tr_b16 v[170:171], v2 offset:28672
	ds_read_b64_tr_b16 v[172:173], v2 offset:29184
	s_waitcnt lgkmcnt(10)
	v_mfma_f32_32x32x16_bf16 v[100:115], v[162:165], v[154:157], v[100:115]
	ds_read_b64_tr_b16 v[124:125], v2 offset:25600
	ds_read_b64_tr_b16 v[126:127], v2 offset:26112
	s_waitcnt lgkmcnt(11)
	v_mfma_f32_32x32x16_bf16 v[82:97], v[174:177], v[150:153], v[82:97]
	ds_read_b64_tr_b16 v[120:121], v2 offset:29696
	ds_read_b64_tr_b16 v[122:123], v2 offset:30208
	s_waitcnt lgkmcnt(12)
	v_mfma_f32_32x32x16_bf16 v[100:115], v[166:169], v[150:153], v[100:115]
	ds_read_b64_tr_b16 v[116:117], v2 offset:26624
	ds_read_b64_tr_b16 v[118:119], v2 offset:27136
	s_waitcnt lgkmcnt(13)
	v_mfma_f32_32x32x16_bf16 v[82:97], v[182:185], v[146:149], v[82:97]
	ds_read_b64_tr_b16 v[12:13], v2 offset:30720
	ds_read_b64_tr_b16 v[14:15], v2 offset:31232
	s_waitcnt lgkmcnt(14)
	v_mfma_f32_32x32x16_bf16 v[100:115], v[178:181], v[146:149], v[100:115]
	ds_read_b64_tr_b16 v[8:9], v2 offset:27648
	ds_read_b64_tr_b16 v[10:11], v2 offset:28160
	s_waitcnt lgkmcnt(14)
	v_mfma_f32_32x32x16_bf16 v[82:97], v[190:193], v[142:145], v[82:97]
	ds_read_b64_tr_b16 v[4:5], v2 offset:31744
	ds_read_b64_tr_b16 v[6:7], v2 offset:32256
	v_mfma_f32_32x32x16_bf16 v[100:115], v[186:189], v[142:145], v[100:115]
	v_or_b32_e32 v17, 0xe0, v239
	v_or_b32_e32 v16, 0xc0, v239
	v_cmp_le_i32_e32 vcc, v17, v238
	s_nop 8
	v_cndmask_b32_e32 v99, v227, v100, vcc
	v_cmp_lt_i32_e32 vcc, v16, v238
	s_nop 1
	v_cndmask_b32_e32 v83, v227, v83, vcc
	v_cmp_le_i32_e32 vcc, v16, v238
	v_or_b32_e32 v16, 0xe1, v239
	s_nop 0
	v_cndmask_b32_e32 v82, v227, v82, vcc
	v_cmp_le_i32_e32 vcc, v16, v238
	v_or_b32_e32 v16, 0xc2, v239
	s_nop 0
	v_cndmask_b32_e32 v100, v227, v101, vcc
	v_cmp_le_i32_e32 vcc, v16, v238
	v_or_b32_e32 v16, 0xe2, v239
	s_nop 0
	v_cndmask_b32_e32 v101, v227, v84, vcc
	v_cmp_le_i32_e32 vcc, v16, v238
	v_or_b32_e32 v16, 0xc3, v239
	s_nop 0
	v_cndmask_b32_e32 v142, v227, v102, vcc
	v_cmp_le_i32_e32 vcc, v16, v238
	v_or_b32_e32 v16, 0xe3, v239
	s_nop 0
	v_cndmask_b32_e32 v143, v227, v85, vcc
	v_cmp_le_i32_e32 vcc, v16, v238
	v_or_b32_e32 v16, 0xc8, v239
	s_nop 0
	v_cndmask_b32_e32 v144, v227, v103, vcc
	v_cmp_le_i32_e32 vcc, v16, v238
	v_or_b32_e32 v16, 0xe8, v239
	s_nop 0
	v_cndmask_b32_e32 v102, v227, v86, vcc
	v_cmp_le_i32_e32 vcc, v16, v238
	v_or_b32_e32 v16, 0xc9, v239
	s_nop 0
	v_cndmask_b32_e32 v86, v227, v104, vcc
	v_cmp_le_i32_e32 vcc, v16, v238
	v_or_b32_e32 v16, 0xe9, v239
	s_nop 0
	v_cndmask_b32_e32 v103, v227, v87, vcc
	v_cmp_le_i32_e32 vcc, v16, v238
	v_or_b32_e32 v16, 0xca, v239
	s_nop 0
	v_cndmask_b32_e32 v87, v227, v105, vcc
	v_cmp_le_i32_e32 vcc, v16, v238
	v_or_b32_e32 v16, 0xea, v239
	s_nop 0
	v_cndmask_b32_e32 v104, v227, v88, vcc
	v_cmp_le_i32_e32 vcc, v16, v238
	v_or_b32_e32 v16, 0xcb, v239
	s_nop 0
	v_cndmask_b32_e32 v88, v227, v106, vcc
	v_cmp_le_i32_e32 vcc, v16, v238
	v_or_b32_e32 v16, 0xeb, v239
	s_nop 0
	v_cndmask_b32_e32 v105, v227, v89, vcc
	v_cmp_le_i32_e32 vcc, v16, v238
	v_or_b32_e32 v16, 0xd0, v239
	s_nop 0
	v_cndmask_b32_e32 v89, v227, v107, vcc
	v_cmp_le_i32_e32 vcc, v16, v238
	v_or_b32_e32 v16, 0xf0, v239
	s_nop 0
	v_cndmask_b32_e32 v106, v227, v90, vcc
	v_cmp_le_i32_e32 vcc, v16, v238
	v_or_b32_e32 v16, 0xd1, v239
	s_nop 0
	v_cndmask_b32_e32 v90, v227, v108, vcc
	v_cmp_le_i32_e32 vcc, v16, v238
	v_or_b32_e32 v16, 0xf1, v239
	s_nop 0
	v_cndmask_b32_e32 v107, v227, v91, vcc
	v_cmp_le_i32_e32 vcc, v16, v238
	v_or_b32_e32 v16, 0xd2, v239
	s_nop 0
	v_cndmask_b32_e32 v91, v227, v109, vcc
	v_cmp_le_i32_e32 vcc, v16, v238
	v_or_b32_e32 v16, 0xf2, v239
	s_nop 0
	v_cndmask_b32_e32 v108, v227, v92, vcc
	v_cmp_le_i32_e32 vcc, v16, v238
	v_or_b32_e32 v16, 0xd3, v239
	s_nop 0
	v_cndmask_b32_e32 v92, v227, v110, vcc
	v_cmp_le_i32_e32 vcc, v16, v238
	v_or_b32_e32 v16, 0xf3, v239
	s_nop 0
	v_cndmask_b32_e32 v109, v227, v93, vcc
	v_cmp_le_i32_e32 vcc, v16, v238
	v_or_b32_e32 v16, 0xd8, v239
	s_nop 0
	v_cndmask_b32_e32 v93, v227, v111, vcc
	v_cmp_le_i32_e32 vcc, v16, v238
	v_or_b32_e32 v16, 0xf8, v239
	s_nop 0
	v_cndmask_b32_e32 v110, v227, v94, vcc
	v_cmp_le_i32_e32 vcc, v16, v238
	v_or_b32_e32 v16, 0xd9, v239
	s_nop 0
	v_cndmask_b32_e32 v94, v227, v112, vcc
	v_cmp_le_i32_e32 vcc, v16, v238
	v_or_b32_e32 v16, 0xf9, v239
	s_nop 0
	v_cndmask_b32_e32 v111, v227, v95, vcc
	v_cmp_le_i32_e32 vcc, v16, v238
	v_or_b32_e32 v16, 0xda, v239
	s_nop 0
	v_cndmask_b32_e32 v95, v227, v113, vcc
	v_cmp_le_i32_e32 vcc, v16, v238
	v_or_b32_e32 v16, 0xfa, v239
	s_nop 0
	v_cndmask_b32_e32 v112, v227, v96, vcc
	v_cmp_le_i32_e32 vcc, v16, v238
	v_or_b32_e32 v16, 0xdb, v239
	s_nop 0
	v_cndmask_b32_e32 v96, v227, v114, vcc
	v_cmp_le_i32_e32 vcc, v16, v238
	v_sub_u32_e32 v16, v238, v239
	v_lshl_add_u32 v145, v16, 2, s40
	v_cndmask_b32_e32 v113, v227, v97, vcc
	v_or_b32_e32 v97, 0xfb, v239
	v_cmp_le_i32_e32 vcc, v97, v238
	ds_read2_b32 v[16:17], v145 offset0:63 offset1:64
	ds_read2_b32 v[84:85], v145 offset0:31 offset1:32
	v_cndmask_b32_e32 v97, v227, v115, vcc
	ds_read2_b32 v[114:115], v145 offset0:61 offset1:62
	ds_read2_b32 v[128:129], v145 offset0:29 offset1:30
	s_waitcnt lgkmcnt(3)
	v_add_f32_e32 v98, v82, v17
	s_waitcnt lgkmcnt(2)
	v_add_f32_e32 v82, v99, v85
	v_add_f32_e32 v99, v83, v16
	v_add_f32_e32 v83, v100, v84
	s_waitcnt lgkmcnt(1)
	v_add_f32_e32 v100, v101, v115
	s_waitcnt lgkmcnt(0)
	v_add_f32_e32 v84, v142, v129
	v_add_f32_e32 v101, v143, v114
	v_add_f32_e32 v85, v144, v128
	s_nop 0
	ds_read2_b32 v[16:17], v145 offset0:55 offset1:56
	ds_read2_b32 v[114:115], v145 offset0:23 offset1:24
	ds_read2_b32 v[128:129], v145 offset0:53 offset1:54
	ds_read2_b32 v[142:143], v145 offset0:21 offset1:22
	s_waitcnt lgkmcnt(3)
	v_add_f32_e32 v102, v102, v17
	s_waitcnt lgkmcnt(2)
	v_add_f32_e32 v86, v86, v115
	v_add_f32_e32 v103, v103, v16
	v_add_f32_e32 v87, v87, v114
	s_waitcnt lgkmcnt(1)
	v_add_f32_e32 v104, v104, v129
	s_waitcnt lgkmcnt(0)
	v_add_f32_e32 v88, v88, v143
	v_add_f32_e32 v105, v105, v128
	v_add_f32_e32 v89, v89, v142
	s_nop 0
	ds_read2_b32 v[16:17], v145 offset0:47 offset1:48
	ds_read2_b32 v[114:115], v145 offset0:15 offset1:16
	ds_read2_b32 v[128:129], v145 offset0:45 offset1:46
	ds_read2_b32 v[142:143], v145 offset0:13 offset1:14
	s_waitcnt lgkmcnt(3)
	v_add_f32_e32 v106, v106, v17
	s_waitcnt lgkmcnt(2)
	v_add_f32_e32 v90, v90, v115
	v_add_f32_e32 v107, v107, v16
	v_add_f32_e32 v91, v91, v114
	s_waitcnt lgkmcnt(1)
	v_add_f32_e32 v108, v108, v129
	s_waitcnt lgkmcnt(0)
	v_add_f32_e32 v92, v92, v143
	v_add_f32_e32 v109, v109, v128
	v_add_f32_e32 v93, v93, v142
	s_nop 0
	ds_read2_b32 v[16:17], v145 offset0:39 offset1:40
	ds_read2_b32 v[114:115], v145 offset0:7 offset1:8
	ds_read2_b32 v[128:129], v145 offset0:37 offset1:38
	ds_read2_b32 v[142:143], v145 offset0:5 offset1:6
	s_waitcnt lgkmcnt(3)
	v_add_f32_e32 v110, v110, v17
	s_waitcnt lgkmcnt(2)
	v_add_f32_e32 v94, v94, v115
	v_add_f32_e32 v111, v111, v16
	v_add_f32_e32 v95, v95, v114
	s_waitcnt lgkmcnt(1)
	v_add_f32_e32 v112, v112, v129
	s_waitcnt lgkmcnt(0)
	v_add_f32_e32 v96, v96, v143
	v_add_f32_e32 v113, v113, v128
	v_add_f32_e32 v97, v97, v142
	s_nop 0
	s_nop 0
	v_max_f32_e32 v16, v99, v98
	v_max3_f32 v17, v100, v101, v83
	v_max3_f32 v16, v16, v82, v84
	v_max3_f32 v16, v16, v85, v102
	v_max3_f32 v17, v17, v104, v105
	v_max3_f32 v16, v16, v103, v86
	v_max3_f32 v17, v17, v88, v89
	v_max3_f32 v16, v16, v87, v106
	v_max3_f32 v17, v17, v108, v109
	v_max3_f32 v16, v16, v107, v90
	v_max3_f32 v17, v17, v92, v93
	v_max3_f32 v16, v16, v91, v110
	v_max3_f32 v17, v17, v112, v113
	v_max3_f32 v16, v16, v111, v94
	v_max3_f32 v17, v17, v96, v97
	v_max3_f32 v16, v16, v95, v17
	v_mov_b32_e32 v17, v16
	s_nop 1
	v_permlane32_swap_b32_e32 v16, v17
	v_max_f32_e32 v16, v16, v17
	v_cmp_lt_f32_e32 vcc, s60, v16
	s_cmp_lg_u64 vcc, 0
	s_cselect_b64 s[0:1], -1, 0
	s_cbranch_vccnz .LBB0_959
